# speedup vs baseline: 1.0274x; 1.0274x over previous
.LBB1_8:
	s_or_b64 exec, exec, s[4:5]
	v_add_u32_e32 v10, v172, v2
	s_waitcnt vmcnt(1) lgkmcnt(0)
	s_barrier
	ds_read_b128 v[18:21], v10 offset:256
	ds_read_b128 v[22:25], v10 offset:288
	ds_read_b128 v[82:85], v10 offset:320
	ds_read_b128 v[86:89], v10 offset:352
	ds_read_b128 v[74:77], v10 offset:384
	ds_read_b128 v[78:81], v10 offset:416
	ds_read_b128 v[2:5], v213 offset:32768
	ds_read_b128 v[6:9], v213 offset:0
	ds_read_b128 v[66:69], v10 offset:448
	ds_read_b128 v[70:73], v10 offset:480
	ds_read_b128 v[10:13], v213 offset:1024
	s_waitcnt lgkmcnt(3)
	v_pk_mul_f32 v[26:27], v[8:9], v[20:21]
	v_pk_mul_f32 v[28:29], v[6:7], v[18:19]
	ds_read_b128 v[14:17], v213 offset:8192
	s_waitcnt lgkmcnt(1)
	v_pk_mul_f32 v[12:13], v[12:13], v[24:25]
	v_pk_mul_f32 v[10:11], v[10:11], v[22:23]
	v_pk_fma_f32 v[30:31], v[8:9], v[20:21], v[12:13]
	v_pk_fma_f32 v[32:33], v[6:7], v[18:19], v[10:11]
	v_cvt_pk_bf16_f32 v9, v12, v13
	v_cvt_pk_bf16_f32 v7, v26, v27
	v_cvt_pk_bf16_f32 v8, v10, v11
	v_cvt_pk_bf16_f32 v6, v28, v29
	ds_read_b128 v[10:13], v213 offset:33792
	s_nop 0
	v_mfma_f32_32x32x16_bf16 v[34:49], v[2:5], v[6:9], 0
	ds_read_b128 v[6:9], v213 offset:9216
	s_waitcnt lgkmcnt(2)
	v_mul_f32_e32 v26, v16, v20
	v_mul_f32_e32 v27, v17, v21
	v_pk_mul_f32 v[50:51], v[14:15], v[18:19]
	s_mov_b32 s4, 0x3727c5ac
	s_waitcnt lgkmcnt(0)
	v_pk_mul_f32 v[8:9], v[8:9], v[24:25]
	v_pk_mul_f32 v[28:29], v[6:7], v[22:23]
	v_pk_fma_f32 v[90:91], v[16:17], v[20:21], v[8:9]
	v_pk_fma_f32 v[92:93], v[14:15], v[18:19], v[28:29]
	ds_read_b128 v[14:17], v213 offset:2048
	v_cvt_pk_bf16_f32 v9, v8, v9
	v_cvt_pk_bf16_f32 v7, v26, v27
	v_cvt_pk_bf16_f32 v8, v28, v29
	ds_read_b128 v[26:29], v213 offset:3072
	v_cvt_pk_bf16_f32 v6, v50, v51
	s_waitcnt lgkmcnt(1)
	v_pk_mul_f32 v[94:95], v[14:15], v[82:83]
	s_mov_b32 s0, 0x3c800000
	v_mfma_f32_32x32x16_bf16 v[50:65], v[2:5], v[6:9], 0
	v_mul_f32_e32 v2, v16, v84
	v_mul_f32_e32 v3, v17, v85
	s_waitcnt lgkmcnt(0)
	v_mul_f32_e32 v4, v28, v88
	v_mul_f32_e32 v5, v29, v89
	v_pk_mul_f32 v[6:7], v[26:27], v[86:87]
	v_pk_fma_f32 v[8:9], v[16:17], v[84:85], v[4:5]
	v_cvt_pk_bf16_f32 v3, v2, v3
	v_pk_fma_f32 v[14:15], v[14:15], v[82:83], v[6:7]
	v_pk_add_f32 v[26:27], v[8:9], v[30:31]
	v_cvt_pk_bf16_f32 v5, v4, v5
	v_cvt_pk_bf16_f32 v4, v6, v7
	ds_read_b128 v[6:9], v213 offset:10240
	v_pk_add_f32 v[28:29], v[14:15], v[32:33]
	ds_read_b128 v[14:17], v213 offset:11264
	v_cvt_pk_bf16_f32 v2, v94, v95
	s_waitcnt lgkmcnt(1)
	v_pk_mul_f32 v[30:31], v[6:7], v[82:83]
	v_mov_b64_e32 v[152:153], s[4:5]
	v_mfma_f32_32x32x16_bf16 v[34:49], v[10:13], v[2:5], v[34:49]
	v_mul_f32_e32 v2, v8, v84
	v_mul_f32_e32 v3, v9, v85
	s_waitcnt lgkmcnt(0)
	v_mul_f32_e32 v4, v16, v88
	v_mul_f32_e32 v5, v17, v89
	v_pk_mul_f32 v[14:15], v[14:15], v[86:87]
	v_pk_fma_f32 v[8:9], v[8:9], v[84:85], v[4:5]
	v_pk_fma_f32 v[6:7], v[6:7], v[82:83], v[14:15]
	v_cvt_pk_bf16_f32 v5, v4, v5
	v_cvt_pk_bf16_f32 v3, v2, v3
	v_cvt_pk_bf16_f32 v4, v14, v15
	v_pk_add_f32 v[32:33], v[8:9], v[90:91]
	v_pk_add_f32 v[90:91], v[6:7], v[92:93]
	ds_read_b128 v[6:9], v213 offset:34816
	ds_read_b128 v[14:17], v213 offset:4096
	v_cvt_pk_bf16_f32 v2, v30, v31
	s_mov_b32 s13, 0
	s_mov_b64 s[6:7], 0
	v_mfma_f32_32x32x16_bf16 v[50:65], v[10:13], v[2:5], v[50:65]
	ds_read_b128 v[2:5], v213 offset:5120
	ds_read_b128 v[10:13], v213 offset:12288
	s_waitcnt lgkmcnt(2)
	v_pk_mul_f32 v[30:31], v[16:17], v[76:77]
	v_pk_mul_f32 v[92:93], v[14:15], v[74:75]
	s_waitcnt lgkmcnt(1)
	v_pk_mul_f32 v[4:5], v[4:5], v[80:81]
	v_pk_mul_f32 v[94:95], v[2:3], v[78:79]
	v_pk_fma_f32 v[2:3], v[16:17], v[76:77], v[4:5]
	v_cvt_pk_bf16_f32 v5, v4, v5
	v_pk_add_f32 v[96:97], v[2:3], v[26:27]
	v_cvt_pk_bf16_f32 v3, v30, v31
	v_cvt_pk_bf16_f32 v4, v94, v95
	v_cvt_pk_bf16_f32 v2, v92, v93
	v_pk_fma_f32 v[14:15], v[14:15], v[74:75], v[94:95]
	s_waitcnt lgkmcnt(0)
	v_pk_mul_f32 v[30:31], v[10:11], v[74:75]
	v_mfma_f32_32x32x16_bf16 v[34:49], v[6:9], v[2:5], v[34:49]
	ds_read_b128 v[2:5], v213 offset:13312
	v_add_f32_e32 v98, v14, v28
	v_add_f32_e32 v99, v15, v29
	ds_read_b128 v[14:17], v213 offset:35840
	v_pk_mul_f32 v[26:27], v[12:13], v[76:77]
	s_waitcnt lgkmcnt(1)
	v_pk_mul_f32 v[4:5], v[4:5], v[80:81]
	v_pk_mul_f32 v[28:29], v[2:3], v[78:79]
	v_pk_fma_f32 v[2:3], v[12:13], v[76:77], v[4:5]
	v_pk_fma_f32 v[10:11], v[10:11], v[74:75], v[28:29]
	v_pk_add_f32 v[32:33], v[2:3], v[32:33]
	v_pk_add_f32 v[92:93], v[10:11], v[90:91]
	ds_read_b128 v[10:13], v213 offset:6144
	v_cvt_pk_bf16_f32 v5, v4, v5
	v_cvt_pk_bf16_f32 v3, v26, v27
	v_cvt_pk_bf16_f32 v4, v28, v29
	ds_read_b128 v[26:29], v213 offset:7168
	v_cvt_pk_bf16_f32 v2, v30, v31
	s_waitcnt lgkmcnt(1)
	v_pk_mul_f32 v[30:31], v[10:11], v[66:67]
	v_mfma_f32_32x32x16_bf16 v[50:65], v[6:9], v[2:5], v[50:65]
	v_mul_f32_e32 v2, v12, v68
	v_mul_f32_e32 v3, v13, v69
	s_waitcnt lgkmcnt(0)
	v_mul_f32_e32 v4, v28, v72
	v_mul_f32_e32 v5, v29, v73
	v_pk_mul_f32 v[6:7], v[26:27], v[70:71]
	v_pk_fma_f32 v[8:9], v[12:13], v[68:69], v[4:5]
	v_cvt_pk_bf16_f32 v3, v2, v3
	v_pk_fma_f32 v[10:11], v[10:11], v[66:67], v[6:7]
	v_pk_add_f32 v[94:95], v[8:9], v[96:97]
	v_cvt_pk_bf16_f32 v5, v4, v5
	v_cvt_pk_bf16_f32 v4, v6, v7
	ds_read_b128 v[6:9], v213 offset:14336
	v_pk_add_f32 v[96:97], v[10:11], v[98:99]
	ds_read_b128 v[10:13], v213 offset:15360
	v_cvt_pk_bf16_f32 v2, v30, v31
	s_waitcnt lgkmcnt(1)
	v_pk_mul_f32 v[30:31], v[6:7], v[66:67]
	v_mfma_f32_32x32x16_bf16 v[34:49], v[14:17], v[2:5], v[34:49]
	s_waitcnt lgkmcnt(0)
	v_mul_f32_e32 v10, v10, v70
	v_mul_f32_e32 v11, v11, v71
	v_mul_f32_e32 v2, v8, v68
	v_mul_f32_e32 v3, v9, v69
	v_pk_mul_f32 v[4:5], v[12:13], v[72:73]
	v_pk_fma_f32 v[6:7], v[6:7], v[66:67], v[10:11]
	v_pk_fma_f32 v[8:9], v[8:9], v[68:69], v[4:5]
	v_pk_add_f32 v[92:93], v[6:7], v[92:93]
	v_cvt_pk_bf16_f32 v3, v2, v3
	v_pk_add_f32 v[90:91], v[8:9], v[32:33]
	v_cvt_pk_bf16_f32 v5, v4, v5
	v_cvt_pk_bf16_f32 v4, v10, v11
	ds_read_b128 v[26:29], v213 offset:36864
	ds_read_b128 v[6:9], v213 offset:16384
	v_cvt_pk_bf16_f32 v2, v30, v31
	ds_read_b128 v[98:101], v213 offset:25600
	ds_read_b128 v[102:105], v213 offset:37888
	v_mfma_f32_32x32x16_bf16 v[50:65], v[14:17], v[2:5], v[50:65]
	ds_read_b128 v[2:5], v213 offset:17408
	ds_read_b128 v[30:33], v213 offset:24576
	s_waitcnt lgkmcnt(4)
	v_pk_mul_f32 v[12:13], v[6:7], v[18:19]
	v_pk_mul_f32 v[10:11], v[8:9], v[20:21]
	s_waitcnt lgkmcnt(1)
	v_pk_mul_f32 v[14:15], v[2:3], v[22:23]
	v_pk_mul_f32 v[22:23], v[98:99], v[22:23]
	v_pk_fma_f32 v[112:113], v[6:7], v[18:19], v[14:15]
	s_waitcnt lgkmcnt(0)
	v_pk_mul_f32 v[114:115], v[30:31], v[18:19]
	v_pk_fma_f32 v[118:119], v[30:31], v[18:19], v[22:23]
	v_pk_mul_f32 v[4:5], v[4:5], v[24:25]
	v_pk_mul_f32 v[106:107], v[32:33], v[20:21]
	v_pk_mul_f32 v[24:25], v[100:101], v[24:25]
	ds_read_b128 v[98:101], v213 offset:18432
	v_cvt_pk_bf16_f32 v19, v106, v107
	ds_read_b128 v[106:109], v213 offset:19456
	v_pk_fma_f32 v[110:111], v[8:9], v[20:21], v[4:5]
	v_cvt_pk_bf16_f32 v5, v4, v5
	v_cvt_pk_bf16_f32 v3, v10, v11
	v_cvt_pk_bf16_f32 v4, v14, v15
	s_waitcnt lgkmcnt(0)
	v_pk_mul_f32 v[106:107], v[106:107], v[86:87]
	v_cvt_pk_bf16_f32 v2, v12, v13
	v_pk_mul_f32 v[120:121], v[98:99], v[82:83]
	v_pk_mul_f32 v[108:109], v[108:109], v[88:89]
	v_pk_fma_f32 v[98:99], v[98:99], v[82:83], v[106:107]
	v_mfma_f32_32x32x16_bf16 v[2:17], v[26:29], v[2:5], 0
	v_cvt_pk_bf16_f32 v18, v114, v115
	v_mul_f32_e32 v114, v100, v84
	v_mul_f32_e32 v115, v101, v85
	v_fma_f32 v100, v100, v84, v108
	v_fma_f32 v101, v101, v85, v109
	v_pk_add_f32 v[124:125], v[98:99], v[112:113]
	v_pk_add_f32 v[122:123], v[100:101], v[110:111]
	v_cvt_pk_bf16_f32 v101, v108, v109
	v_cvt_pk_bf16_f32 v100, v106, v107
	ds_read_b128 v[106:109], v213 offset:26624
	v_pk_fma_f32 v[116:117], v[32:33], v[20:21], v[24:25]
	v_cvt_pk_bf16_f32 v21, v24, v25
	v_cvt_pk_bf16_f32 v20, v22, v23
	ds_read_b128 v[110:113], v213 offset:27648
	v_cvt_pk_bf16_f32 v99, v114, v115
	v_mfma_f32_32x32x16_bf16 v[18:33], v[26:29], v[18:21], 0
	v_cvt_pk_bf16_f32 v98, v120, v121
	s_waitcnt lgkmcnt(1)
	v_mul_f32_e32 v114, v106, v82
	v_mul_f32_e32 v115, v107, v83
	s_waitcnt lgkmcnt(0)
	v_pk_mul_f32 v[86:87], v[110:111], v[86:87]
	v_pk_mul_f32 v[88:89], v[112:113], v[88:89]
	v_pk_fma_f32 v[82:83], v[106:107], v[82:83], v[86:87]
	v_mfma_f32_32x32x16_bf16 v[2:17], v[102:105], v[98:101], v[2:17]
	v_mul_f32_e32 v98, v108, v84
	v_mul_f32_e32 v99, v109, v85
	v_fma_f32 v84, v108, v84, v88
	v_fma_f32 v85, v109, v85, v89
	v_add_f32_e32 v108, v82, v118
	v_add_f32_e32 v109, v83, v119
	v_cvt_pk_bf16_f32 v83, v98, v99
	v_pk_add_f32 v[106:107], v[84:85], v[116:117]
	v_cvt_pk_bf16_f32 v85, v88, v89
	v_cvt_pk_bf16_f32 v84, v86, v87
	ds_read_b128 v[86:89], v213 offset:38912
	ds_read_b128 v[98:101], v213 offset:20480
	v_cvt_pk_bf16_f32 v82, v114, v115
	s_waitcnt lgkmcnt(0)
	v_pk_mul_f32 v[110:111], v[100:101], v[76:77]
	v_mfma_f32_32x32x16_bf16 v[18:33], v[102:105], v[82:85], v[18:33]
	ds_read_b128 v[82:85], v213 offset:21504
	ds_read_b128 v[102:105], v213 offset:28672
	v_mul_f32_e32 v112, v98, v74
	v_mul_f32_e32 v113, v99, v75
	s_waitcnt lgkmcnt(1)
	v_pk_mul_f32 v[84:85], v[84:85], v[80:81]
	v_pk_mul_f32 v[114:115], v[82:83], v[78:79]
	v_pk_fma_f32 v[82:83], v[100:101], v[76:77], v[84:85]
	v_cvt_pk_bf16_f32 v85, v84, v85
	v_pk_add_f32 v[116:117], v[82:83], v[122:123]
	v_cvt_pk_bf16_f32 v83, v110, v111
	v_cvt_pk_bf16_f32 v84, v114, v115
	v_cvt_pk_bf16_f32 v82, v112, v113
	v_pk_fma_f32 v[98:99], v[98:99], v[74:75], v[114:115]
	s_waitcnt lgkmcnt(0)
	v_pk_mul_f32 v[112:113], v[102:103], v[74:75]
	v_mfma_f32_32x32x16_bf16 v[2:17], v[86:89], v[82:85], v[2:17]
	ds_read_b128 v[82:85], v213 offset:29696
	v_add_f32_e32 v118, v98, v124
	v_add_f32_e32 v119, v99, v125
	v_mul_f32_e32 v110, v104, v76
	v_mul_f32_e32 v111, v105, v77
	ds_read_b128 v[98:101], v213 offset:39936
	s_waitcnt lgkmcnt(1)
	v_pk_mul_f32 v[78:79], v[82:83], v[78:79]
	v_pk_mul_f32 v[80:81], v[84:85], v[80:81]
	v_pk_fma_f32 v[74:75], v[102:103], v[74:75], v[78:79]
	v_pk_fma_f32 v[76:77], v[104:105], v[76:77], v[80:81]
	v_pk_add_f32 v[104:105], v[74:75], v[108:109]
	v_pk_add_f32 v[102:103], v[76:77], v[106:107]
	v_cvt_pk_bf16_f32 v77, v80, v81
	v_cvt_pk_bf16_f32 v76, v78, v79
	ds_read_b128 v[78:81], v213 offset:22528
	ds_read_b128 v[82:85], v213 offset:23552
	v_cvt_pk_bf16_f32 v75, v110, v111
	v_cvt_pk_bf16_f32 v74, v112, v113
	s_waitcnt lgkmcnt(0)
	v_pk_mul_f32 v[82:83], v[82:83], v[70:71]
	v_mfma_f32_32x32x16_bf16 v[18:33], v[86:89], v[74:77], v[18:33]
	v_mul_f32_e32 v74, v80, v68
	v_mul_f32_e32 v75, v81, v69
	v_mul_f32_e32 v76, v84, v72
	v_mul_f32_e32 v77, v85, v73
	v_mul_f32_e32 v86, v78, v66
	v_mul_f32_e32 v87, v79, v67
	v_pk_fma_f32 v[80:81], v[80:81], v[68:69], v[76:77]
	v_pk_fma_f32 v[78:79], v[78:79], v[66:67], v[82:83]
	v_cvt_pk_bf16_f32 v75, v74, v75
	v_pk_add_f32 v[88:89], v[80:81], v[116:117]
	v_pk_add_f32 v[106:107], v[78:79], v[118:119]
	ds_read_b128 v[78:81], v213 offset:30720
	v_cvt_pk_bf16_f32 v77, v76, v77
	v_cvt_pk_bf16_f32 v76, v82, v83
	ds_read_b128 v[82:85], v213 offset:31744
	v_cvt_pk_bf16_f32 v74, v86, v87
	s_waitcnt lgkmcnt(0)
	v_pk_mul_f32 v[72:73], v[84:85], v[72:73]
	v_mfma_f32_32x32x16_bf16 v[2:17], v[98:101], v[74:77], v[2:17]
	v_mul_f32_e32 v74, v80, v68
	v_mul_f32_e32 v75, v81, v69
	v_fma_f32 v68, v80, v68, v72
	v_fma_f32 v69, v81, v69, v73
	v_mul_f32_e32 v70, v82, v70
	v_mul_f32_e32 v71, v83, v71
	v_pk_add_f32 v[84:85], v[68:69], v[102:103]
	v_cvt_pk_bf16_f32 v69, v72, v73
	v_pk_mov_b32 v[72:73], v[96:97], v[94:95] op_sel:[1,0]
	v_mov_b32_e32 v97, v95
	v_pk_add_f32 v[72:73], v[72:73], v[96:97]
	v_pk_mul_f32 v[76:77], v[78:79], v[66:67]
	v_pk_fma_f32 v[66:67], v[78:79], v[66:67], v[70:71]
	v_pk_add_f32 v[72:73], v[72:73], v[72:73] op_sel:[0,1] op_sel_hi:[1,0]
	v_pk_add_f32 v[86:87], v[66:67], v[104:105]
	v_mov_b32_e32 v66, v72
	s_nop 1
	v_permlane32_swap_b32_e32 v72, v66
	v_add_f32_e32 v66, v72, v66
	v_cvt_pk_bf16_f32 v67, v74, v75
	v_rcp_f32_e32 v74, v66
	v_cvt_pk_bf16_f32 v68, v70, v71
	v_cvt_pk_bf16_f32 v66, v76, v77
	v_pk_mul_f32 v[70:71], v[46:47], v[74:75] op_sel_hi:[1,0]
	s_nop 0
	v_mfma_f32_32x32x16_bf16 v[18:33], v[98:101], v[66:69], v[18:33]
	v_mul_f32_e32 v66, v42, v74
	v_mul_f32_e32 v67, v43, v74
	v_pk_mov_b32 v[42:43], v[92:93], v[90:91] op_sel:[1,0]
	v_mov_b32_e32 v93, v91
	v_pk_add_f32 v[42:43], v[42:43], v[92:93]
	v_pk_mul_f32 v[68:69], v[44:45], v[74:75] op_sel_hi:[1,0]
	v_pk_add_f32 v[42:43], v[42:43], v[42:43] op_sel:[0,1] op_sel_hi:[1,0]
	v_pk_mov_b32 v[44:45], v[106:107], v[88:89] op_sel:[1,0]
	v_mov_b32_e32 v43, v42
	s_nop 1
	v_permlane32_swap_b32_e32 v42, v43
	v_add_f32_e32 v42, v42, v43
	v_rcp_f32_e32 v42, v42
	v_mov_b32_e32 v107, v89
	v_pk_add_f32 v[44:45], v[44:45], v[106:107]
	v_pk_mul_f32 v[72:73], v[48:49], v[74:75] op_sel_hi:[1,0]
	v_pk_add_f32 v[44:45], v[44:45], v[44:45] op_sel:[0,1] op_sel_hi:[1,0]
	v_pk_mul_f32 v[36:37], v[36:37], v[74:75] op_sel_hi:[1,0]
	v_pk_mul_f32 v[38:39], v[38:39], v[74:75] op_sel_hi:[1,0]
	v_pk_mul_f32 v[40:41], v[40:41], v[74:75] op_sel_hi:[1,0]
	v_pk_mul_f32 v[34:35], v[34:35], v[74:75] op_sel_hi:[1,0]
	v_pk_mul_f32 v[74:75], v[58:59], v[42:43] op_sel_hi:[1,0]
	v_pk_mul_f32 v[78:79], v[60:61], v[42:43] op_sel_hi:[1,0]
	v_pk_mul_f32 v[80:81], v[62:63], v[42:43] op_sel_hi:[1,0]
	v_pk_mul_f32 v[82:83], v[64:65], v[42:43] op_sel_hi:[1,0]
	v_pk_mul_f32 v[92:93], v[52:53], v[42:43] op_sel_hi:[1,0]
	v_mov_b32_e32 v43, v44
	s_nop 1
	v_permlane32_swap_b32_e32 v44, v43
	v_add_f32_e32 v43, v44, v43
	v_rcp_f32_e32 v76, v43
	v_pk_mul_f32 v[96:97], v[54:55], v[42:43] op_sel_hi:[1,0]
	v_pk_mul_f32 v[94:95], v[56:57], v[42:43] op_sel_hi:[1,0]
	v_pk_mul_f32 v[98:99], v[50:51], v[42:43] op_sel_hi:[1,0]
	v_pk_mul_f32 v[100:101], v[4:5], v[76:77] op_sel_hi:[1,0]
	v_pk_mov_b32 v[4:5], v[86:87], v[84:85] op_sel:[1,0]
	v_mov_b32_e32 v87, v85
	v_pk_add_f32 v[4:5], v[4:5], v[86:87]
	v_pk_mul_f32 v[102:103], v[6:7], v[76:77] op_sel_hi:[1,0]
	v_pk_add_f32 v[104:105], v[4:5], v[4:5] op_sel:[0,1] op_sel_hi:[1,0]
	v_cvt_pk_bf16_f32 v7, v40, v41
	ds_read_b128 v[84:87], v150 offset:52224
	ds_read_b128 v[50:53], v150 offset:35840
	ds_read_b128 v[54:57], v150 offset:36864
	ds_read_b128 v[58:61], v150 offset:37888
	ds_read_b128 v[62:65], v150 offset:38912
	v_cvt_pk_bf16_f32 v6, v38, v39
	v_cvt_pk_bf16_f32 v5, v36, v37
	v_cvt_pk_bf16_f32 v4, v34, v35
	ds_read_b128 v[88:91], v150 offset:53248
	ds_read_b128 v[34:37], v150 offset:39936
	ds_read_b128 v[38:41], v150 offset:40960
	ds_read_b128 v[42:45], v150 offset:41984
	ds_read_b128 v[46:49], v150 offset:43008
	v_cvt_pk_bf16_f32 v95, v94, v95
	v_cvt_pk_bf16_f32 v94, v96, v97
	v_cvt_pk_bf16_f32 v93, v92, v93
	v_cvt_pk_bf16_f32 v92, v98, v99
	s_waitcnt lgkmcnt(5)
	v_mfma_f32_32x32x16_bf16 v[50:65], v[84:87], v[4:7], v[50:65]
	v_mul_f32_e32 v10, v10, v76
	v_mul_f32_e32 v11, v11, v76
	v_mul_f32_e32 v12, v12, v76
	v_mul_f32_e32 v13, v13, v76
	v_mul_f32_e32 v8, v8, v76
	v_mul_f32_e32 v9, v9, v76
	v_mov_b32_e32 v77, v104
	s_nop 1
	v_permlane32_swap_b32_e32 v104, v77
	v_cvt_pk_bf16_f32 v73, v72, v73
	s_waitcnt lgkmcnt(0)
	v_mfma_f32_32x32x16_bf16 v[34:49], v[84:87], v[92:95], v[34:49]
	v_cvt_pk_bf16_f32 v72, v70, v71
	v_cvt_pk_bf16_f32 v70, v66, v67
	v_add_f32_e32 v66, v104, v77
	v_cvt_pk_bf16_f32 v71, v68, v69
	v_rcp_f32_e32 v104, v66
	v_cvt_pk_bf16_f32 v69, v82, v83
	v_cvt_pk_bf16_f32 v68, v80, v81
	v_cvt_pk_bf16_f32 v67, v78, v79
	v_cvt_pk_bf16_f32 v66, v74, v75
	ds_read_b128 v[78:81], v150 offset:54272
	v_mfma_f32_32x32x16_bf16 v[50:65], v[88:91], v[70:73], v[50:65]
	v_mul_f32_e32 v2, v2, v76
	v_mul_f32_e32 v3, v3, v76
	v_mul_f32_e32 v20, v20, v104
	v_mul_f32_e32 v21, v21, v104
	v_cvt_pk_bf16_f32 v85, v8, v9
	v_cvt_pk_bf16_f32 v82, v2, v3
	v_pk_mul_f32 v[2:3], v[22:23], v[104:105] op_sel_hi:[1,0]
	v_pk_mul_f32 v[8:9], v[24:25], v[104:105] op_sel_hi:[1,0]
	v_pk_mul_f32 v[18:19], v[18:19], v[104:105] op_sel_hi:[1,0]
	v_mfma_f32_32x32x16_bf16 v[34:49], v[88:91], v[66:69], v[34:49]
	v_cvt_pk_bf16_f32 v84, v102, v103
	v_cvt_pk_bf16_f32 v83, v100, v101
	ds_read_b128 v[86:89], v150 offset:55296
	v_cvt_pk_bf16_f32 v99, v8, v9
	v_cvt_pk_bf16_f32 v98, v2, v3
	v_cvt_pk_bf16_f32 v97, v20, v21
	v_cvt_pk_bf16_f32 v96, v18, v19
	s_waitcnt lgkmcnt(1)
	v_mfma_f32_32x32x16_bf16 v[50:65], v[78:81], v[82:85], v[50:65]
	v_mul_f32_e32 v2, v14, v76
	v_mul_f32_e32 v3, v15, v76
	v_mul_f32_e32 v8, v16, v76
	v_mul_f32_e32 v9, v17, v76
	v_mul_f32_e32 v14, v26, v104
	v_mul_f32_e32 v15, v27, v104
	v_cvt_pk_bf16_f32 v77, v8, v9
	v_cvt_pk_bf16_f32 v76, v2, v3
	v_cvt_pk_bf16_f32 v74, v10, v11
	v_pk_mul_f32 v[2:3], v[28:29], v[104:105] op_sel_hi:[1,0]
	v_mfma_f32_32x32x16_bf16 v[34:49], v[78:81], v[96:99], v[34:49]
	v_mul_f32_e32 v8, v30, v104
	v_mul_f32_e32 v9, v31, v104
	v_mul_f32_e32 v10, v32, v104
	v_mul_f32_e32 v11, v33, v104
	v_cvt_pk_bf16_f32 v75, v12, v13
	v_cvt_pk_bf16_f32 v81, v10, v11
	v_cvt_pk_bf16_f32 v80, v8, v9
	v_cvt_pk_bf16_f32 v79, v2, v3
	v_cvt_pk_bf16_f32 v78, v14, v15
	s_waitcnt lgkmcnt(0)
	v_mfma_f32_32x32x16_bf16 v[50:65], v[86:89], v[74:77], v[50:65]
	v_mfma_f32_32x32x16_bf16 v[34:49], v[86:89], v[78:81], v[34:49]
	ds_read_b128 v[86:89], v150 offset:56320
	ds_read_b128 v[18:21], v150 offset:44032
	ds_read_b128 v[22:25], v150 offset:45056
	ds_read_b128 v[26:29], v150 offset:46080
	ds_read_b128 v[30:33], v150 offset:47104
	ds_read_b128 v[100:103], v150 offset:57344
	s_waitcnt lgkmcnt(1)
	v_mfma_f32_32x32x16_bf16 v[18:33], v[86:89], v[4:7], v[18:33]
	ds_read_b128 v[2:5], v150 offset:48128
	ds_read_b128 v[6:9], v150 offset:49152
	ds_read_b128 v[10:13], v150 offset:50176
	ds_read_b128 v[14:17], v150 offset:51200
	s_waitcnt lgkmcnt(0)
	v_mfma_f32_32x32x16_bf16 v[2:17], v[86:89], v[92:95], v[2:17]
	v_mfma_f32_32x32x16_bf16 v[18:33], v[100:103], v[70:73], v[18:33]
	v_mfma_f32_32x32x16_bf16 v[2:17], v[100:103], v[66:69], v[2:17]
	ds_read_b128 v[66:69], v150 offset:58368
	ds_read_b128 v[70:73], v150 offset:59392
	s_waitcnt lgkmcnt(1)
	v_mfma_f32_32x32x16_bf16 v[18:33], v[66:69], v[82:85], v[18:33]
	v_mfma_f32_32x32x16_bf16 v[2:17], v[66:69], v[96:99], v[2:17]
	s_waitcnt lgkmcnt(0)
	v_mfma_f32_32x32x16_bf16 v[18:33], v[70:73], v[74:77], v[18:33]
	v_mfma_f32_32x32x16_bf16 v[2:17], v[70:73], v[78:81], v[2:17]
	s_nop 10
	v_mul_f32_e32 v66, v22, v22
	v_mul_f32_e32 v67, v23, v23
	v_mul_f32_e32 v68, v30, v30
	v_mul_f32_e32 v69, v31, v31
	v_mul_f32_e32 v70, v24, v24
	v_mul_f32_e32 v71, v25, v25
	v_pk_mul_f32 v[72:73], v[32:33], v[32:33]
	v_pk_mul_f32 v[74:75], v[20:21], v[20:21]
	v_pk_mul_f32 v[76:77], v[28:29], v[28:29]
	v_pk_mul_f32 v[78:79], v[26:27], v[26:27]
	v_pk_mul_f32 v[80:81], v[18:19], v[18:19]
	v_pk_fma_f32 v[78:79], v[58:59], v[58:59], v[78:79]
	v_pk_fma_f32 v[76:77], v[60:61], v[60:61], v[76:77]
	v_pk_fma_f32 v[74:75], v[52:53], v[52:53], v[74:75]
	v_pk_fma_f32 v[72:73], v[64:65], v[64:65], v[72:73]
	v_pk_fma_f32 v[70:71], v[56:57], v[56:57], v[70:71]
	v_pk_fma_f32 v[68:69], v[62:63], v[62:63], v[68:69]
	v_pk_fma_f32 v[66:67], v[54:55], v[54:55], v[66:67]
	v_pk_fma_f32 v[80:81], v[50:51], v[50:51], v[80:81]
	v_pk_add_f32 v[66:67], v[66:67], v[68:69]
	v_pk_add_f32 v[68:69], v[70:71], v[72:73]
	v_pk_add_f32 v[70:71], v[74:75], v[76:77]
	v_pk_add_f32 v[72:73], v[80:81], v[78:79]
	v_pk_add_f32 v[68:69], v[70:71], v[68:69]
	v_pk_add_f32 v[66:67], v[72:73], v[66:67]
	v_pk_mul_f32 v[72:73], v[14:15], v[14:15]
	v_pk_mov_b32 v[70:71], v[66:67], v[68:69] op_sel:[1,0]
	v_mov_b32_e32 v67, v69
	v_pk_add_f32 v[66:67], v[70:71], v[66:67]
	v_pk_mul_f32 v[70:71], v[6:7], v[6:7]
	v_pk_mul_f32 v[74:75], v[8:9], v[8:9]
	v_pk_mul_f32 v[76:77], v[16:17], v[16:17]
	v_pk_mul_f32 v[78:79], v[4:5], v[4:5]
	v_pk_mul_f32 v[80:81], v[12:13], v[12:13]
	v_pk_mul_f32 v[82:83], v[10:11], v[10:11]
	v_pk_mul_f32 v[84:85], v[2:3], v[2:3]
	v_pk_fma_f32 v[82:83], v[42:43], v[42:43], v[82:83]
	v_pk_fma_f32 v[80:81], v[44:45], v[44:45], v[80:81]
	v_pk_fma_f32 v[78:79], v[36:37], v[36:37], v[78:79]
	v_pk_fma_f32 v[76:77], v[48:49], v[48:49], v[76:77]
	v_pk_fma_f32 v[74:75], v[40:41], v[40:41], v[74:75]
	v_pk_fma_f32 v[72:73], v[46:47], v[46:47], v[72:73]
	v_pk_fma_f32 v[70:71], v[38:39], v[38:39], v[70:71]
	v_pk_fma_f32 v[84:85], v[34:35], v[34:35], v[84:85]
	v_pk_add_f32 v[70:71], v[70:71], v[72:73]
	v_pk_add_f32 v[72:73], v[74:75], v[76:77]
	v_pk_add_f32 v[74:75], v[78:79], v[80:81]
	v_pk_add_f32 v[76:77], v[84:85], v[82:83]
	v_pk_add_f32 v[72:73], v[74:75], v[72:73]
	v_pk_add_f32 v[70:71], v[76:77], v[70:71]
	v_pk_add_f32 v[66:67], v[66:67], v[66:67] op_sel:[0,1] op_sel_hi:[1,0]
	v_pk_mov_b32 v[74:75], v[70:71], v[72:73] op_sel:[1,0]
	v_mov_b32_e32 v71, v73
	v_pk_add_f32 v[70:71], v[74:75], v[70:71]
	v_mov_b32_e32 v69, v66
	v_pk_add_f32 v[70:71], v[70:71], v[70:71] op_sel:[0,1] op_sel_hi:[1,0]
	s_nop 0
	v_permlane32_swap_b32_e32 v66, v69
	v_mov_b32_e32 v68, v70
	s_nop 1
	v_permlane32_swap_b32_e32 v70, v68
	v_mov_b32_e32 v71, v66
	v_pk_add_f32 v[66:67], v[70:71], v[68:69]
	v_pk_fma_f32 v[66:67], v[66:67], s[0:1], v[152:153] op_sel_hi:[1,0,0]
	s_mov_b32 s1, 0x800000
	v_mul_f32_e32 v68, 0x4b800000, v67
	v_cmp_gt_f32_e32 vcc, s1, v67
	s_nop 1
	v_cndmask_b32_e32 v67, v67, v68, vcc
	v_rsq_f32_e32 v67, v67
	s_nop 0
	v_mul_f32_e32 v68, 0x45800000, v67
	v_cndmask_b32_e32 v68, v67, v68, vcc
	v_pk_mul_f32 v[158:159], v[50:51], v[68:69] op_sel_hi:[1,0]
	v_pk_mul_f32 v[50:51], v[18:19], v[68:69] op_sel_hi:[1,0]
	v_mul_f32_e32 v18, 0x4b800000, v66
	v_cmp_gt_f32_e32 vcc, s1, v66
	v_pk_mul_f32 v[80:81], v[60:61], v[68:69] op_sel_hi:[1,0]
	v_pk_mul_f32 v[60:61], v[28:29], v[68:69] op_sel_hi:[1,0]
	v_cndmask_b32_e32 v18, v66, v18, vcc
	v_rsq_f32_e32 v18, v18
	v_pk_mul_f32 v[78:79], v[58:59], v[68:69] op_sel_hi:[1,0]
	v_pk_mul_f32 v[160:161], v[52:53], v[68:69] op_sel_hi:[1,0]
	v_pk_mul_f32 v[82:83], v[54:55], v[68:69] op_sel_hi:[1,0]
	v_mul_f32_e32 v19, 0x45800000, v18
	v_cndmask_b32_e32 v28, v18, v19, vcc
	v_pk_mul_f32 v[168:169], v[56:57], v[68:69] op_sel_hi:[1,0]
	v_pk_mul_f32 v[58:59], v[26:27], v[68:69] op_sel_hi:[1,0]
	v_pk_mul_f32 v[52:53], v[20:21], v[68:69] op_sel_hi:[1,0]
	v_pk_mul_f32 v[54:55], v[22:23], v[68:69] op_sel_hi:[1,0]
	v_pk_mul_f32 v[56:57], v[24:25], v[68:69] op_sel_hi:[1,0]
	v_pk_mul_f32 v[18:19], v[42:43], v[28:29] op_sel_hi:[1,0]
	v_pk_mul_f32 v[20:21], v[44:45], v[28:29] op_sel_hi:[1,0]
	v_pk_mul_f32 v[22:23], v[46:47], v[28:29] op_sel_hi:[1,0]
	v_pk_mul_f32 v[26:27], v[48:49], v[28:29] op_sel_hi:[1,0]
	v_pk_mul_f32 v[162:163], v[34:35], v[28:29] op_sel_hi:[1,0]
	v_pk_mul_f32 v[164:165], v[36:37], v[28:29] op_sel_hi:[1,0]
	v_pk_mul_f32 v[166:167], v[38:39], v[28:29] op_sel_hi:[1,0]
	v_pk_mul_f32 v[24:25], v[40:41], v[28:29] op_sel_hi:[1,0]
	v_pk_mul_f32 v[104:105], v[2:3], v[28:29] op_sel_hi:[1,0]
	v_pk_mul_f32 v[112:113], v[4:5], v[28:29] op_sel_hi:[1,0]
	ds_read_b128 v[2:5], v150 offset:60416
	ds_read_b128 v[34:37], v174 offset:32768
	ds_read_b128 v[38:41], v174 offset:32800
	ds_read_b128 v[42:45], v174 offset:32832
	ds_read_b128 v[46:49], v174 offset:32864
	v_cvt_pk_bf16_f32 v129, v168, v169
	v_cvt_pk_bf16_f32 v128, v82, v83
	v_cvt_pk_bf16_f32 v127, v160, v161
	v_cvt_pk_bf16_f32 v126, v158, v159
	v_cvt_pk_bf16_f32 v137, v24, v25
	v_cvt_pk_bf16_f32 v136, v166, v167
	v_cvt_pk_bf16_f32 v135, v164, v165
	s_waitcnt lgkmcnt(0)
	v_mfma_f32_32x32x16_bf16 v[86:101], v[2:5], v[126:129], v[34:49]
	v_cvt_pk_bf16_f32 v134, v162, v163
	v_mul_f32_e32 v84, v62, v68
	v_mul_f32_e32 v85, v63, v68
	v_mul_f32_e32 v170, v64, v68
	v_mul_f32_e32 v171, v65, v68
	v_pk_mul_f32 v[62:63], v[30:31], v[68:69] op_sel_hi:[1,0]
	v_pk_mul_f32 v[64:65], v[32:33], v[68:69] op_sel_hi:[1,0]
	v_pk_mul_f32 v[116:117], v[6:7], v[28:29] op_sel_hi:[1,0]
	v_pk_mul_f32 v[154:155], v[8:9], v[28:29] op_sel_hi:[1,0]
	v_mfma_f32_32x32x16_bf16 v[34:49], v[2:5], v[134:137], v[34:49]
	ds_read_b128 v[6:9], v150 offset:61440
	ds_read_b128 v[66:69], v174 offset:32896
	ds_read_b128 v[106:109], v150 offset:64512
	v_cvt_pk_bf16_f32 v125, v170, v171
	v_cvt_pk_bf16_f32 v124, v84, v85
	v_cvt_pk_bf16_f32 v123, v80, v81
	v_cvt_pk_bf16_f32 v122, v78, v79
	v_cvt_pk_bf16_f32 v149, v26, v27
	v_cvt_pk_bf16_f32 v148, v22, v23
	v_cvt_pk_bf16_f32 v147, v20, v21
	v_cvt_pk_bf16_f32 v146, v18, v19
	s_waitcnt lgkmcnt(2)
	v_mfma_f32_32x32x16_bf16 v[86:101], v[6:9], v[122:125], v[86:101]
	v_mul_f32_e32 v102, v10, v28
	v_mul_f32_e32 v103, v11, v28
	v_mul_f32_e32 v110, v12, v28
	v_mul_f32_e32 v111, v13, v28
	v_mul_f32_e32 v114, v14, v28
	v_mul_f32_e32 v115, v15, v28
	v_pk_mul_f32 v[156:157], v[16:17], v[28:29] op_sel_hi:[1,0]
	ds_read_b128 v[176:179], v174 offset:33536
	ds_read_b128 v[180:183], v174 offset:33568
	ds_read_b128 v[184:187], v174 offset:33600
	ds_read_b128 v[28:31], v174 offset:33632
	ds_read_b128 v[188:191], v174 offset:33792
	ds_read_b128 v[192:195], v174 offset:33824
	ds_read_b128 v[196:199], v174 offset:33856
	ds_read_b128 v[200:203], v174 offset:33888
	ds_read_b128 v[204:207], v150 offset:62464
	v_cvt_pk_bf16_f32 v133, v56, v57
	v_mfma_f32_32x32x16_bf16 v[34:49], v[6:9], v[146:149], v[34:49]
	v_cvt_pk_bf16_f32 v132, v54, v55
	v_cvt_pk_bf16_f32 v131, v52, v53
	v_cvt_pk_bf16_f32 v130, v50, v51
	ds_read_b128 v[70:73], v174 offset:33664
	ds_read_b128 v[74:77], v174 offset:33920
	ds_read_b128 v[208:211], v150 offset:63488
	v_cvt_pk_bf16_f32 v145, v154, v155
	v_cvt_pk_bf16_f32 v144, v116, v117
	v_cvt_pk_bf16_f32 v143, v112, v113
	v_cvt_pk_bf16_f32 v142, v104, v105
	s_waitcnt lgkmcnt(3)
	v_mfma_f32_32x32x16_bf16 v[86:101], v[204:207], v[130:133], v[86:101]
	v_cvt_pk_bf16_f32 v121, v64, v65
	v_cvt_pk_bf16_f32 v120, v62, v63
	v_cvt_pk_bf16_f32 v119, v60, v61
	v_cvt_pk_bf16_f32 v118, v58, v59
	v_cvt_pk_bf16_f32 v141, v156, v157
	v_cvt_pk_bf16_f32 v140, v114, v115
	v_cvt_pk_bf16_f32 v139, v110, v111
	v_mfma_f32_32x32x16_bf16 v[34:49], v[204:207], v[142:145], v[34:49]
	v_cvt_pk_bf16_f32 v138, v102, v103
	v_fma_f32 v16, v30, v170, v202
	v_fma_f32 v17, v31, v171, v203
	v_fma_f32 v14, v28, v84, v200
	v_fma_f32 v15, v29, v85, v201
	v_pk_fma_f32 v[12:13], v[186:187], v[80:81], v[198:199]
	v_pk_fma_f32 v[10:11], v[184:185], v[78:79], v[196:197]
	v_pk_fma_f32 v[8:9], v[182:183], v[168:169], v[194:195]
	s_waitcnt lgkmcnt(0)
	v_mfma_f32_32x32x16_bf16 v[86:101], v[208:211], v[118:121], v[86:101]
	v_fma_f32 v6, v180, v82, v192
	v_fma_f32 v7, v181, v83, v193
	ds_read_b128 v[78:81], v174 offset:33760
	ds_read_b128 v[82:85], v174 offset:33248
	v_fma_f32 v4, v178, v160, v190
	v_fma_f32 v5, v179, v161, v191
	v_pk_fma_f32 v[2:3], v[176:177], v[158:159], v[188:189]
	v_pk_fma_f32 v[32:33], v[30:31], v[26:27], v[202:203]
	v_pk_fma_f32 v[30:31], v[28:29], v[22:23], v[200:201]
	v_pk_fma_f32 v[28:29], v[186:187], v[20:21], v[198:199]
	v_pk_fma_f32 v[26:27], v[184:185], v[18:19], v[196:197]
	v_pk_fma_f32 v[24:25], v[182:183], v[24:25], v[194:195]
	v_pk_fma_f32 v[22:23], v[180:181], v[166:167], v[192:193]
	v_pk_fma_f32 v[20:21], v[178:179], v[164:165], v[190:191]
	v_pk_fma_f32 v[18:19], v[176:177], v[162:163], v[188:189]
	ds_read_b128 v[158:161], v174 offset:33696
	ds_read_b128 v[162:165], v174 offset:33728
	ds_read_b128 v[166:169], v174 offset:33952
	ds_read_b128 v[176:179], v174 offset:33984
	ds_read_b128 v[180:183], v174 offset:34016
	ds_read_b128 v[184:187], v212 offset:11264
	v_mfma_f32_32x32x16_bf16 v[34:49], v[208:211], v[138:141], v[34:49]
	v_cvt_pk_bf16_f32 v86, v86, v87
	v_cvt_pk_bf16_f32 v87, v88, v89
	v_cvt_pk_bf16_f32 v88, v90, v91
	v_cvt_pk_bf16_f32 v89, v92, v93
	ds_read_b128 v[90:93], v212 offset:12288
	v_pk_max_i16 v86, v86, 0
	v_pk_max_i16 v87, v87, 0
	v_pk_max_i16 v88, v88, 0
	v_pk_max_i16 v89, v89, 0
	s_nop 1
	s_nop 0
	v_cvt_pk_bf16_f32 v188, v34, v35
	v_cvt_pk_bf16_f32 v189, v36, v37
	v_cvt_pk_bf16_f32 v190, v38, v39
	v_cvt_pk_bf16_f32 v191, v40, v41
	s_waitcnt lgkmcnt(1)
	v_mfma_f32_32x32x16_bf16 v[2:17], v[184:187], v[86:89], v[2:17]
	v_pk_max_i16 v188, v188, 0
	v_pk_max_i16 v189, v189, 0
	v_pk_max_i16 v190, v190, 0
	v_pk_max_i16 v191, v191, 0
	v_cvt_pk_bf16_f32 v94, v94, v95
	v_cvt_pk_bf16_f32 v95, v96, v97
	v_cvt_pk_bf16_f32 v96, v98, v99
	v_cvt_pk_bf16_f32 v97, v100, v101
	v_cvt_pk_bf16_f32 v98, v42, v43
	v_cvt_pk_bf16_f32 v99, v44, v45
	v_mfma_f32_32x32x16_bf16 v[18:33], v[184:187], v[188:191], v[18:33]
	ds_read_b128 v[184:187], v212 offset:19456
	v_cvt_pk_bf16_f32 v100, v46, v47
	v_cvt_pk_bf16_f32 v101, v48, v49
	v_fma_f32 v64, v80, v64, v182
	v_fma_f32 v65, v81, v65, v183
	v_pk_fma_f32 v[62:63], v[78:79], v[62:63], v[180:181]
	v_pk_fma_f32 v[60:61], v[164:165], v[60:61], v[178:179]
	v_pk_fma_f32 v[58:59], v[162:163], v[58:59], v[176:177]
	v_pk_max_i16 v94, v94, 0
	v_pk_max_i16 v95, v95, 0
	v_pk_max_i16 v96, v96, 0
	v_pk_max_i16 v97, v97, 0
	v_pk_max_i16 v98, v98, 0
	v_pk_max_i16 v99, v99, 0
	v_pk_max_i16 v100, v100, 0
	v_pk_max_i16 v101, v101, 0
	v_pk_fma_f32 v[56:57], v[160:161], v[56:57], v[168:169]
	s_waitcnt lgkmcnt(1)
	v_mfma_f32_32x32x16_bf16 v[2:17], v[90:93], v[94:97], v[2:17]
	v_fma_f32 v54, v158, v54, v166
	v_fma_f32 v55, v159, v55, v167
	v_fma_f32 v52, v72, v52, v76
	v_fma_f32 v53, v73, v53, v77
	v_fma_f32 v50, v70, v50, v74
	v_fma_f32 v51, v71, v51, v75
	v_pk_fma_f32 v[48:49], v[80:81], v[156:157], v[182:183]
	v_pk_fma_f32 v[46:47], v[78:79], v[114:115], v[180:181]
	v_pk_fma_f32 v[44:45], v[164:165], v[110:111], v[178:179]
	v_pk_fma_f32 v[42:43], v[162:163], v[102:103], v[176:177]
	v_mfma_f32_32x32x16_bf16 v[18:33], v[90:93], v[98:101], v[18:33]
	ds_read_b128 v[90:93], v212 offset:20480
	v_fma_f32 v40, v160, v154, v168
	v_fma_f32 v41, v161, v155, v169
	v_fma_f32 v38, v158, v116, v166
	v_fma_f32 v39, v159, v117, v167
	v_pk_fma_f32 v[36:37], v[72:73], v[112:113], v[76:77]
	v_pk_fma_f32 v[34:35], v[70:71], v[104:105], v[74:75]
	s_waitcnt lgkmcnt(1)
	v_mfma_f32_32x32x16_bf16 v[50:65], v[184:187], v[86:89], v[50:65]
	ds_read_b128 v[70:73], v174 offset:32928
	ds_read_b128 v[74:77], v174 offset:32960
	ds_read_b128 v[78:81], v174 offset:32992
	ds_read_b128 v[86:89], v174 offset:33024
	ds_read_b128 v[110:113], v212 offset:1024
	v_mfma_f32_32x32x16_bf16 v[34:49], v[184:187], v[188:191], v[34:49]
	s_waitcnt lgkmcnt(5)
	v_mfma_f32_32x32x16_bf16 v[50:65], v[90:93], v[94:97], v[50:65]
	v_mfma_f32_32x32x16_bf16 v[34:49], v[90:93], v[98:101], v[34:49]
	s_waitcnt lgkmcnt(2)
	v_mfma_f32_32x32x16_bf16 v[90:105], v[106:109], v[126:129], v[66:81]
	v_mfma_f32_32x32x16_bf16 v[66:81], v[106:109], v[134:137], v[66:81]
	ds_read_b128 v[106:109], v212 offset:0
	s_waitcnt lgkmcnt(0)
	v_mfma_f32_32x32x16_bf16 v[90:105], v[106:109], v[122:125], v[90:105]
	v_mfma_f32_32x32x16_bf16 v[66:81], v[106:109], v[146:149], v[66:81]
	ds_read_b128 v[106:109], v212 offset:2048
	v_mfma_f32_32x32x16_bf16 v[90:105], v[110:113], v[130:133], v[90:105]
	v_mfma_f32_32x32x16_bf16 v[66:81], v[110:113], v[142:145], v[66:81]
	ds_read_b128 v[110:113], v212 offset:13312
	s_waitcnt lgkmcnt(1)
	v_mfma_f32_32x32x16_bf16 v[90:105], v[106:109], v[118:121], v[90:105]
	v_mfma_f32_32x32x16_bf16 v[66:81], v[106:109], v[138:141], v[66:81]
	s_nop 10
	v_cvt_pk_bf16_f32 v90, v90, v91
	v_cvt_pk_bf16_f32 v91, v92, v93
	v_cvt_pk_bf16_f32 v92, v94, v95
	v_cvt_pk_bf16_f32 v94, v98, v99
	v_cvt_pk_bf16_f32 v95, v100, v101
	ds_read_b128 v[98:101], v212 offset:21504
	v_cvt_pk_bf16_f32 v66, v66, v67
	v_cvt_pk_bf16_f32 v67, v68, v69
	v_cvt_pk_bf16_f32 v68, v70, v71
	v_cvt_pk_bf16_f32 v93, v96, v97
	v_cvt_pk_bf16_f32 v69, v72, v73
	ds_read_b128 v[70:73], v212 offset:14336
	v_pk_max_i16 v90, v90, 0
	v_pk_max_i16 v91, v91, 0
	v_pk_max_i16 v92, v92, 0
	v_pk_max_i16 v93, v93, 0
	v_pk_max_i16 v66, v66, 0
	v_pk_max_i16 v67, v67, 0
	v_pk_max_i16 v68, v68, 0
	v_pk_max_i16 v69, v69, 0
	v_cvt_pk_bf16_f32 v96, v102, v103
	s_waitcnt lgkmcnt(2)
	v_mfma_f32_32x32x16_bf16 v[2:17], v[110:113], v[90:93], v[2:17]
	v_cvt_pk_bf16_f32 v97, v104, v105
	v_cvt_pk_bf16_f32 v74, v74, v75
	v_cvt_pk_bf16_f32 v75, v76, v77
	v_cvt_pk_bf16_f32 v76, v78, v79
	v_cvt_pk_bf16_f32 v77, v80, v81
	v_pk_max_i16 v94, v94, 0
	v_pk_max_i16 v95, v95, 0
	v_pk_max_i16 v96, v96, 0
	v_pk_max_i16 v97, v97, 0
	v_pk_max_i16 v74, v74, 0
	v_pk_max_i16 v75, v75, 0
	v_pk_max_i16 v76, v76, 0
	v_pk_max_i16 v77, v77, 0
	v_mfma_f32_32x32x16_bf16 v[18:33], v[110:113], v[66:69], v[18:33]
	s_waitcnt lgkmcnt(1)
	v_mfma_f32_32x32x16_bf16 v[34:49], v[98:101], v[66:69], v[34:49]
	ds_read_b128 v[66:69], v212 offset:22528
	v_mfma_f32_32x32x16_bf16 v[50:65], v[98:101], v[90:93], v[50:65]
	s_waitcnt lgkmcnt(1)
	v_mfma_f32_32x32x16_bf16 v[2:17], v[70:73], v[94:97], v[2:17]
	v_mfma_f32_32x32x16_bf16 v[18:33], v[70:73], v[74:77], v[18:33]
	ds_read_b128 v[78:81], v212 offset:3072
	s_waitcnt lgkmcnt(1)
	v_mfma_f32_32x32x16_bf16 v[50:65], v[66:69], v[94:97], v[50:65]
	ds_read_b128 v[90:93], v174 offset:33056
	ds_read_b128 v[94:97], v174 offset:33088
	ds_read_b128 v[98:101], v174 offset:33120
	ds_read_b128 v[70:73], v174 offset:33152
	v_mfma_f32_32x32x16_bf16 v[34:49], v[66:69], v[74:77], v[34:49]
	ds_read_b128 v[66:69], v212 offset:4096
	ds_read_b128 v[74:77], v212 offset:5120
	s_waitcnt lgkmcnt(3)
	v_mfma_f32_32x32x16_bf16 v[102:117], v[78:81], v[126:129], v[86:101]
	v_mfma_f32_32x32x16_bf16 v[86:101], v[78:81], v[134:137], v[86:101]
	s_waitcnt lgkmcnt(1)
	v_mfma_f32_32x32x16_bf16 v[86:101], v[66:69], v[146:149], v[86:101]
	v_mfma_f32_32x32x16_bf16 v[102:117], v[66:69], v[122:125], v[102:117]
	ds_read_b128 v[66:69], v212 offset:6144
	s_waitcnt lgkmcnt(1)
	v_mfma_f32_32x32x16_bf16 v[86:101], v[74:77], v[142:145], v[86:101]
	v_mfma_f32_32x32x16_bf16 v[102:117], v[74:77], v[130:133], v[102:117]
	ds_read_b128 v[74:77], v212 offset:15360
	s_waitcnt lgkmcnt(1)
	v_mfma_f32_32x32x16_bf16 v[86:101], v[66:69], v[138:141], v[86:101]
	v_mfma_f32_32x32x16_bf16 v[102:117], v[66:69], v[118:121], v[102:117]
	s_nop 10
	v_cvt_pk_bf16_f32 v78, v86, v87
	v_cvt_pk_bf16_f32 v80, v90, v91
	v_cvt_pk_bf16_f32 v79, v88, v89
	v_cvt_pk_bf16_f32 v81, v92, v93
	ds_read_b128 v[86:89], v212 offset:16384
	ds_read_b128 v[90:93], v212 offset:23552
	v_cvt_pk_bf16_f32 v66, v102, v103
	v_cvt_pk_bf16_f32 v67, v104, v105
	v_cvt_pk_bf16_f32 v68, v106, v107
	v_cvt_pk_bf16_f32 v69, v108, v109
	v_pk_max_i16 v66, v66, 0
	v_pk_max_i16 v67, v67, 0
	v_pk_max_i16 v68, v68, 0
	v_pk_max_i16 v69, v69, 0
	v_pk_max_i16 v78, v78, 0
	v_pk_max_i16 v79, v79, 0
	v_pk_max_i16 v80, v80, 0
	v_pk_max_i16 v81, v81, 0
	v_cvt_pk_bf16_f32 v94, v94, v95
	s_waitcnt lgkmcnt(2)
	v_mfma_f32_32x32x16_bf16 v[18:33], v[74:77], v[78:81], v[18:33]
	v_cvt_pk_bf16_f32 v95, v96, v97
	v_cvt_pk_bf16_f32 v96, v98, v99
	v_cvt_pk_bf16_f32 v97, v100, v101
	v_pk_max_i16 v94, v94, 0
	v_pk_max_i16 v95, v95, 0
	v_pk_max_i16 v96, v96, 0
	v_pk_max_i16 v97, v97, 0
	v_mfma_f32_32x32x16_bf16 v[2:17], v[74:77], v[66:69], v[2:17]
	v_cvt_pk_bf16_f32 v74, v110, v111
	v_cvt_pk_bf16_f32 v75, v112, v113
	v_cvt_pk_bf16_f32 v76, v114, v115
	v_cvt_pk_bf16_f32 v77, v116, v117
	v_pk_max_i16 v74, v74, 0
	v_pk_max_i16 v75, v75, 0
	v_pk_max_i16 v76, v76, 0
	v_pk_max_i16 v77, v77, 0
	s_waitcnt lgkmcnt(0)
	v_mfma_f32_32x32x16_bf16 v[50:65], v[90:93], v[66:69], v[50:65]
	ds_read_b128 v[66:69], v212 offset:24576
	v_mfma_f32_32x32x16_bf16 v[34:49], v[90:93], v[78:81], v[34:49]
	ds_read_b128 v[102:105], v212 offset:7168
	v_mfma_f32_32x32x16_bf16 v[2:17], v[86:89], v[74:77], v[2:17]
	s_waitcnt lgkmcnt(1)
	v_mfma_f32_32x32x16_bf16 v[50:65], v[66:69], v[74:77], v[50:65]
	ds_read_b128 v[74:77], v174 offset:33184
	ds_read_b128 v[78:81], v174 offset:33216
	v_mfma_f32_32x32x16_bf16 v[34:49], v[66:69], v[94:97], v[34:49]
	ds_read_b128 v[66:69], v212 offset:8192
	v_mfma_f32_32x32x16_bf16 v[18:33], v[86:89], v[94:97], v[18:33]
	s_waitcnt lgkmcnt(1)
	v_mfma_f32_32x32x16_bf16 v[86:101], v[102:105], v[126:129], v[70:85]
	v_mfma_f32_32x32x16_bf16 v[70:85], v[102:105], v[134:137], v[70:85]
	ds_read_b128 v[102:105], v212 offset:9216
	v_lshlrev_b32_e32 v135, 2, v1
	v_add_u32_e32 v134, v172, v174
	s_waitcnt lgkmcnt(1)
	v_mfma_f32_32x32x16_bf16 v[86:101], v[66:69], v[122:125], v[86:101]
	v_mfma_f32_32x32x16_bf16 v[70:85], v[66:69], v[146:149], v[70:85]
	ds_read_b128 v[66:69], v212 offset:10240
	s_waitcnt lgkmcnt(1)
	v_mfma_f32_32x32x16_bf16 v[86:101], v[102:105], v[130:133], v[86:101]
	v_mfma_f32_32x32x16_bf16 v[70:85], v[102:105], v[142:145], v[70:85]
	ds_read_b128 v[102:105], v212 offset:17408
	s_waitcnt lgkmcnt(1)
	v_mfma_f32_32x32x16_bf16 v[86:101], v[66:69], v[118:121], v[86:101]
	v_mfma_f32_32x32x16_bf16 v[70:85], v[66:69], v[138:141], v[70:85]
	s_nop 10
	v_cvt_pk_bf16_f32 v68, v90, v91
	v_cvt_pk_bf16_f32 v69, v92, v93
	ds_read_b128 v[90:93], v212 offset:25600
	v_cvt_pk_bf16_f32 v66, v86, v87
	v_cvt_pk_bf16_f32 v67, v88, v89
	v_pk_max_i16 v66, v66, 0
	v_pk_max_i16 v67, v67, 0
	v_pk_max_i16 v68, v68, 0
	v_pk_max_i16 v69, v69, 0
	v_cvt_pk_bf16_f32 v70, v70, v71
	v_cvt_pk_bf16_f32 v71, v72, v73
	s_waitcnt lgkmcnt(1)
	v_mfma_f32_32x32x16_bf16 v[2:17], v[102:105], v[66:69], v[2:17]
	v_cvt_pk_bf16_f32 v72, v74, v75
	v_cvt_pk_bf16_f32 v73, v76, v77
	ds_read_b128 v[74:77], v212 offset:18432
	v_cvt_pk_bf16_f32 v86, v94, v95
	v_cvt_pk_bf16_f32 v87, v96, v97
	v_cvt_pk_bf16_f32 v88, v98, v99
	s_waitcnt lgkmcnt(1)
	v_mfma_f32_32x32x16_bf16 v[50:65], v[90:93], v[66:69], v[50:65]
	ds_read_b128 v[66:69], v212 offset:26624
	v_cvt_pk_bf16_f32 v89, v100, v101
	v_pk_max_i16 v86, v86, 0
	v_pk_max_i16 v87, v87, 0
	v_pk_max_i16 v88, v88, 0
	v_pk_max_i16 v89, v89, 0
	v_pk_max_i16 v70, v70, 0
	v_pk_max_i16 v71, v71, 0
	v_pk_max_i16 v72, v72, 0
	v_pk_max_i16 v73, v73, 0
	v_cvt_pk_bf16_f32 v78, v78, v79
	v_cvt_pk_bf16_f32 v79, v80, v81
	s_waitcnt lgkmcnt(1)
	v_mfma_f32_32x32x16_bf16 v[2:17], v[74:77], v[86:89], v[2:17]
	v_cvt_pk_bf16_f32 v80, v82, v83
	v_cvt_pk_bf16_f32 v81, v84, v85
	v_pk_max_i16 v78, v78, 0
	v_pk_max_i16 v79, v79, 0
	v_pk_max_i16 v80, v80, 0
	v_pk_max_i16 v81, v81, 0
	s_waitcnt lgkmcnt(0)
	v_mfma_f32_32x32x16_bf16 v[50:65], v[66:69], v[86:89], v[50:65]
	v_mfma_f32_32x32x16_bf16 v[34:49], v[90:93], v[70:73], v[34:49]
	s_nop 10
	v_add_f32_e32 v130, v10, v58
	v_add_f32_e32 v131, v11, v59
	v_add_f32_e32 v132, v12, v60
	v_add_f32_e32 v133, v13, v61
	v_add_f32_e32 v138, v4, v52
	v_add_f32_e32 v139, v5, v53
	v_pk_add_f32 v[140:141], v[16:17], v[64:65]
	v_pk_add_f32 v[142:143], v[8:9], v[56:57]
	v_pk_add_f32 v[144:145], v[14:15], v[62:63]
	v_pk_add_f32 v[146:147], v[6:7], v[54:55]
	v_mfma_f32_32x32x16_bf16 v[18:33], v[102:105], v[70:73], v[18:33]
	ds_read2st64_b32 v[70:71], v135 offset0:133 offset1:134
	v_add_f32_e32 v148, v2, v50
	v_add_f32_e32 v149, v3, v51
	v_add_f32_e32 v144, v146, v144
	v_add_f32_e32 v145, v147, v145
	v_pk_add_f32 v[140:141], v[142:143], v[140:141]
	v_pk_add_f32 v[132:133], v[138:139], v[132:133]
	v_pk_add_f32 v[130:131], v[148:149], v[130:131]
	v_pk_add_f32 v[132:133], v[132:133], v[140:141]
	v_pk_add_f32 v[130:131], v[130:131], v[144:145]
	v_mfma_f32_32x32x16_bf16 v[34:49], v[66:69], v[78:81], v[34:49]
	v_pk_mov_b32 v[138:139], v[130:131], v[132:133] op_sel:[1,0]
	v_mov_b32_e32 v131, v133
	s_waitcnt vmcnt(0) lgkmcnt(0)
	v_mul_f32_e32 v66, v175, v70
	v_pk_add_f32 v[130:131], v[138:139], v[130:131]
	ds_write_b32 v173, v66 offset:512
	v_mul_f32_e32 v66, v175, v71
	v_pk_add_f32 v[130:131], v[130:131], v[130:131] op_sel:[0,1] op_sel_hi:[1,0]
	s_waitcnt lgkmcnt(0)
	ds_read_b128 v[102:105], v174 offset:34560
	ds_read_b128 v[98:101], v174 offset:34592
	ds_read_b128 v[110:113], v174 offset:34624
	ds_read_b128 v[106:109], v174 offset:34656
	ds_read_b128 v[114:117], v174 offset:34688
	ds_read_b128 v[122:125], v174 offset:34720
	ds_read_b128 v[118:121], v174 offset:34752
	ds_read_b128 v[126:129], v174 offset:34784
	v_mov_b32_dpp v66, v66 quad_perm:[1,0,3,2] row_mask:0xf bank_mask:0xf bound_ctrl:1
	v_mov_b32_e32 v131, v130
	v_fmac_f32_e32 v66, v175, v71
	s_nop 0
	v_permlane32_swap_b32_e32 v130, v131
	v_add_f32_dpp v66, v66, v66 quad_perm:[2,3,0,1] row_mask:0xf bank_mask:0xf bound_ctrl:1
	v_add_f32_e32 v130, v130, v131
	v_fmamk_f32 v65, v130, 0xbc800000, v65
	v_add_f32_dpp v66, v66, v66 row_half_mirror row_mask:0xf bank_mask:0xf bound_ctrl:1
	v_fmamk_f32 v64, v130, 0xbc800000, v64
	v_fmamk_f32 v63, v130, 0xbc800000, v63
	v_fmamk_f32 v62, v130, 0xbc800000, v62
	v_fmamk_f32 v61, v130, 0xbc800000, v61
	v_fmamk_f32 v60, v130, 0xbc800000, v60
	v_fmamk_f32 v59, v130, 0xbc800000, v59
	v_fmamk_f32 v58, v130, 0xbc800000, v58
	v_fmamk_f32 v57, v130, 0xbc800000, v57
	v_fmamk_f32 v56, v130, 0xbc800000, v56
	v_fmamk_f32 v55, v130, 0xbc800000, v55
	v_fmamk_f32 v54, v130, 0xbc800000, v54
	v_fmamk_f32 v53, v130, 0xbc800000, v53
	v_fmamk_f32 v52, v130, 0xbc800000, v52
	v_fmamk_f32 v51, v130, 0xbc800000, v51
	v_fmac_f32_e32 v50, 0xbc800000, v130
	v_add_f32_dpp v66, v66, v66 row_ror:8 row_mask:0xf bank_mask:0xf bound_ctrl:1
	v_fmamk_f32 v17, v130, 0xbc800000, v17
	v_fmamk_f32 v16, v130, 0xbc800000, v16
	v_fmamk_f32 v15, v130, 0xbc800000, v15
	v_fmamk_f32 v14, v130, 0xbc800000, v14
	v_fmamk_f32 v13, v130, 0xbc800000, v13
	v_fmamk_f32 v12, v130, 0xbc800000, v12
	v_fmamk_f32 v11, v130, 0xbc800000, v11
	v_fmamk_f32 v10, v130, 0xbc800000, v10
	v_fmamk_f32 v9, v130, 0xbc800000, v9
	v_fmamk_f32 v8, v130, 0xbc800000, v8
	v_fmamk_f32 v7, v130, 0xbc800000, v7
	v_fmamk_f32 v6, v130, 0xbc800000, v6
	v_fmamk_f32 v5, v130, 0xbc800000, v5
	v_fmamk_f32 v4, v130, 0xbc800000, v4
	v_fmamk_f32 v3, v130, 0xbc800000, v3
	v_fmac_f32_e32 v2, 0xbc800000, v130
	v_pk_mul_f32 v[130:131], v[54:55], v[54:55]
	v_pk_mul_f32 v[132:133], v[62:63], v[62:63]
	v_pk_mul_f32 v[138:139], v[50:51], v[50:51]
	v_pk_mul_f32 v[140:141], v[58:59], v[58:59]
	v_pk_mul_f32 v[142:143], v[56:57], v[56:57]
	v_pk_mul_f32 v[144:145], v[64:65], v[64:65]
	v_pk_mul_f32 v[146:147], v[52:53], v[52:53]
	v_pk_mul_f32 v[148:149], v[60:61], v[60:61]
	v_mov_b32_e32 v67, v66
	v_pk_fma_f32 v[148:149], v[12:13], v[12:13], v[148:149]
	v_pk_fma_f32 v[146:147], v[4:5], v[4:5], v[146:147]
	v_pk_fma_f32 v[144:145], v[16:17], v[16:17], v[144:145]
	v_pk_fma_f32 v[142:143], v[8:9], v[8:9], v[142:143]
	v_pk_fma_f32 v[140:141], v[10:11], v[10:11], v[140:141]
	v_pk_fma_f32 v[138:139], v[2:3], v[2:3], v[138:139]
	v_pk_fma_f32 v[132:133], v[14:15], v[14:15], v[132:133]
	v_pk_fma_f32 v[130:131], v[6:7], v[6:7], v[130:131]
	v_permlane16_swap_b32_e32 v66, v67
	v_pk_add_f32 v[130:131], v[130:131], v[132:133]
	v_pk_add_f32 v[132:133], v[138:139], v[140:141]
	v_pk_add_f32 v[138:139], v[142:143], v[144:145]
	v_pk_add_f32 v[140:141], v[146:147], v[148:149]
	v_mfma_f32_32x32x16_bf16 v[18:33], v[74:77], v[78:81], v[18:33]
	v_add_f32_e32 v136, v66, v67
	ds_read_b128 v[70:73], v134 offset:512
	ds_read_b128 v[66:69], v134 offset:544
	ds_read_b128 v[78:81], v134 offset:576
	ds_read_b128 v[74:77], v134 offset:608
	ds_read_b128 v[82:85], v134 offset:640
	ds_read_b128 v[90:93], v134 offset:672
	ds_read_b128 v[86:89], v134 offset:704
	ds_read_b128 v[94:97], v134 offset:736
	v_pk_add_f32 v[138:139], v[140:141], v[138:139]
	v_pk_add_f32 v[130:131], v[132:133], v[130:131]
	s_waitcnt lgkmcnt(8)
	v_pk_mul_f32 v[140:141], v[126:127], v[62:63]
	v_pk_mov_b32 v[132:133], v[130:131], v[138:139] op_sel:[1,0]
	v_mov_b32_e32 v131, v139
	v_pk_mul_f32 v[138:139], v[122:123], v[54:55]
	v_pk_mul_f32 v[142:143], v[114:115], v[50:51]
	v_pk_mul_f32 v[144:145], v[118:119], v[58:59]
	v_pk_mul_f32 v[146:147], v[124:125], v[56:57]
	v_pk_mul_f32 v[148:149], v[128:129], v[64:65]
	v_pk_mul_f32 v[154:155], v[116:117], v[52:53]
	v_pk_mul_f32 v[156:157], v[120:121], v[60:61]
	v_pk_fma_f32 v[154:155], v[104:105], v[4:5], v[154:155]
	v_pk_fma_f32 v[156:157], v[112:113], v[12:13], v[156:157]
	v_pk_fma_f32 v[148:149], v[108:109], v[16:17], v[148:149]
	v_pk_fma_f32 v[146:147], v[100:101], v[8:9], v[146:147]
	v_pk_fma_f32 v[144:145], v[110:111], v[10:11], v[144:145]
	v_pk_fma_f32 v[142:143], v[102:103], v[2:3], v[142:143]
	v_pk_fma_f32 v[140:141], v[106:107], v[14:15], v[140:141]
	v_pk_fma_f32 v[138:139], v[98:99], v[6:7], v[138:139]
	v_pk_add_f32 v[130:131], v[132:133], v[130:131]
	v_pk_add_f32 v[138:139], v[138:139], v[140:141]
	v_pk_add_f32 v[140:141], v[142:143], v[144:145]
	v_pk_add_f32 v[142:143], v[146:147], v[148:149]
	v_pk_add_f32 v[144:145], v[154:155], v[156:157]
	v_pk_add_f32 v[132:133], v[130:131], v[130:131] op_sel:[0,1] op_sel_hi:[1,0]
	v_pk_add_f32 v[142:143], v[144:145], v[142:143]
	v_pk_add_f32 v[138:139], v[140:141], v[138:139]
	v_add_f32_e32 v133, v142, v143
	v_add_f32_e32 v130, v138, v139
	s_waitcnt lgkmcnt(2)
	v_pk_mul_f32 v[138:139], v[90:91], v[54:55]
	s_waitcnt lgkmcnt(0)
	v_pk_mul_f32 v[140:141], v[94:95], v[62:63]
	v_pk_mul_f32 v[142:143], v[82:83], v[50:51]
	v_pk_mul_f32 v[144:145], v[86:87], v[58:59]
	v_pk_mul_f32 v[146:147], v[92:93], v[56:57]
	v_pk_mul_f32 v[148:149], v[96:97], v[64:65]
	v_pk_mul_f32 v[154:155], v[84:85], v[52:53]
	v_pk_mul_f32 v[156:157], v[88:89], v[60:61]
	v_add_f32_e32 v130, v130, v133
	v_pk_fma_f32 v[156:157], v[80:81], v[12:13], v[156:157]
	v_pk_fma_f32 v[154:155], v[72:73], v[4:5], v[154:155]
	v_pk_fma_f32 v[148:149], v[76:77], v[16:17], v[148:149]
	v_pk_fma_f32 v[146:147], v[68:69], v[8:9], v[146:147]
	v_pk_fma_f32 v[144:145], v[78:79], v[10:11], v[144:145]
	v_pk_fma_f32 v[142:143], v[70:71], v[2:3], v[142:143]
	v_pk_fma_f32 v[140:141], v[74:75], v[14:15], v[140:141]
	v_pk_fma_f32 v[138:139], v[66:67], v[6:7], v[138:139]
	v_mov_b32_e32 v133, v130
	v_pk_add_f32 v[138:139], v[138:139], v[140:141]
	v_pk_add_f32 v[140:141], v[142:143], v[144:145]
	v_pk_add_f32 v[142:143], v[146:147], v[148:149]
	v_pk_add_f32 v[144:145], v[154:155], v[156:157]
	v_permlane32_swap_b32_e32 v130, v133
	v_pk_add_f32 v[142:143], v[144:145], v[142:143]
	v_add_f32_e32 v160, v130, v133
	v_pk_add_f32 v[138:139], v[140:141], v[138:139]
	v_add_f32_e32 v133, v142, v143
	v_pk_add_f32 v[140:141], v[26:27], v[42:43]
	v_pk_add_f32 v[142:143], v[28:29], v[44:45]
	v_pk_add_f32 v[144:145], v[20:21], v[36:37]
	v_pk_add_f32 v[146:147], v[32:33], v[48:49]
	v_pk_add_f32 v[148:149], v[24:25], v[40:41]
	v_pk_add_f32 v[154:155], v[30:31], v[46:47]
	v_pk_add_f32 v[156:157], v[22:23], v[38:39]
	v_pk_add_f32 v[158:159], v[18:19], v[34:35]
	v_pk_add_f32 v[154:155], v[156:157], v[154:155]
	v_pk_add_f32 v[146:147], v[148:149], v[146:147]
	v_pk_add_f32 v[142:143], v[144:145], v[142:143]
	v_pk_add_f32 v[140:141], v[158:159], v[140:141]
	v_pk_add_f32 v[142:143], v[142:143], v[146:147]
	v_pk_add_f32 v[140:141], v[140:141], v[154:155]
	v_add_f32_e32 v130, v138, v139
	v_pk_mov_b32 v[144:145], v[140:141], v[142:143] op_sel:[1,0]
	v_mov_b32_e32 v141, v143
	v_pk_add_f32 v[140:141], v[144:145], v[140:141]
	v_add_f32_e32 v133, v130, v133
	v_pk_add_f32 v[140:141], v[140:141], v[140:141] op_sel:[0,1] op_sel_hi:[1,0]
	v_mov_b32_e32 v131, v132
	v_mov_b32_e32 v130, v140
	s_nop 1
	v_permlane32_swap_b32_e32 v140, v130
	v_add_f32_e32 v130, v140, v130
	v_fmamk_f32 v49, v130, 0xbc800000, v49
	v_fmamk_f32 v48, v130, 0xbc800000, v48
	v_fmamk_f32 v47, v130, 0xbc800000, v47
	v_fmamk_f32 v46, v130, 0xbc800000, v46
	v_fmamk_f32 v45, v130, 0xbc800000, v45
	v_fmamk_f32 v44, v130, 0xbc800000, v44
	v_fmamk_f32 v43, v130, 0xbc800000, v43
	v_fmamk_f32 v42, v130, 0xbc800000, v42
	v_fmamk_f32 v41, v130, 0xbc800000, v41
	v_fmamk_f32 v40, v130, 0xbc800000, v40
	v_fmamk_f32 v39, v130, 0xbc800000, v39
	v_fmamk_f32 v38, v130, 0xbc800000, v38
	v_fmamk_f32 v37, v130, 0xbc800000, v37
	v_fmamk_f32 v36, v130, 0xbc800000, v36
	v_fmamk_f32 v35, v130, 0xbc800000, v35
	v_fmac_f32_e32 v34, 0xbc800000, v130
	v_fmamk_f32 v33, v130, 0xbc800000, v33
	v_fmamk_f32 v32, v130, 0xbc800000, v32
	v_fmamk_f32 v31, v130, 0xbc800000, v31
	v_fmamk_f32 v30, v130, 0xbc800000, v30
	v_fmamk_f32 v29, v130, 0xbc800000, v29
	v_fmamk_f32 v28, v130, 0xbc800000, v28
	v_fmamk_f32 v27, v130, 0xbc800000, v27
	v_fmamk_f32 v26, v130, 0xbc800000, v26
	v_fmamk_f32 v25, v130, 0xbc800000, v25
	v_fmamk_f32 v24, v130, 0xbc800000, v24
	v_fmamk_f32 v23, v130, 0xbc800000, v23
	v_fmamk_f32 v22, v130, 0xbc800000, v22
	v_fmamk_f32 v21, v130, 0xbc800000, v21
	v_fmamk_f32 v20, v130, 0xbc800000, v20
	v_fmamk_f32 v19, v130, 0xbc800000, v19
	v_fmac_f32_e32 v18, 0xbc800000, v130
	v_pk_mul_f32 v[140:141], v[38:39], v[38:39]
	v_pk_mul_f32 v[142:143], v[46:47], v[46:47]
	v_pk_mul_f32 v[144:145], v[34:35], v[34:35]
	v_pk_mul_f32 v[146:147], v[42:43], v[42:43]
	v_pk_mul_f32 v[148:149], v[40:41], v[40:41]
	v_pk_mul_f32 v[154:155], v[48:49], v[48:49]
	v_pk_mul_f32 v[156:157], v[36:37], v[36:37]
	v_pk_mul_f32 v[158:159], v[44:45], v[44:45]
	v_pk_fma_f32 v[156:157], v[20:21], v[20:21], v[156:157]
	v_pk_fma_f32 v[158:159], v[28:29], v[28:29], v[158:159]
	v_pk_fma_f32 v[154:155], v[32:33], v[32:33], v[154:155]
	v_pk_fma_f32 v[148:149], v[24:25], v[24:25], v[148:149]
	v_pk_fma_f32 v[146:147], v[26:27], v[26:27], v[146:147]
	v_pk_fma_f32 v[144:145], v[18:19], v[18:19], v[144:145]
	v_pk_fma_f32 v[142:143], v[30:31], v[30:31], v[142:143]
	v_pk_fma_f32 v[140:141], v[22:23], v[22:23], v[140:141]
	v_permlane32_swap_b32_e32 v132, v131
	v_pk_add_f32 v[140:141], v[140:141], v[142:143]
	v_pk_add_f32 v[142:143], v[144:145], v[146:147]
	v_pk_add_f32 v[144:145], v[148:149], v[154:155]
	v_pk_add_f32 v[146:147], v[156:157], v[158:159]
	v_pk_add_f32 v[140:141], v[142:143], v[140:141]
	v_pk_add_f32 v[144:145], v[146:147], v[144:145]
	v_pk_mul_f32 v[122:123], v[122:123], v[38:39]
	v_pk_mov_b32 v[142:143], v[140:141], v[144:145] op_sel:[1,0]
	v_mov_b32_e32 v141, v145
	v_pk_add_f32 v[140:141], v[142:143], v[140:141]
	v_pk_mul_f32 v[126:127], v[126:127], v[46:47]
	v_pk_add_f32 v[140:141], v[140:141], v[140:141] op_sel:[0,1] op_sel_hi:[1,0]
	v_pk_mul_f32 v[114:115], v[114:115], v[34:35]
	v_mov_b32_e32 v130, v140
	s_nop 1
	v_permlane32_swap_b32_e32 v140, v130
	v_mov_b32_e32 v141, v132
	v_pk_add_f32 v[130:131], v[140:141], v[130:131]
	v_pk_mul_f32 v[118:119], v[118:119], v[42:43]
	v_pk_fma_f32 v[130:131], v[130:131], s[0:1], v[152:153] op_sel_hi:[1,0,0]
	v_pk_mul_f32 v[124:125], v[124:125], v[40:41]
	v_mul_f32_e32 v132, 0x4b800000, v131
	v_cmp_gt_f32_e32 vcc, s1, v131
	v_pk_mul_f32 v[128:129], v[128:129], v[48:49]
	v_pk_mul_f32 v[116:117], v[116:117], v[36:37]
	v_pk_mul_f32 v[120:121], v[120:121], v[44:45]
	v_cndmask_b32_e32 v131, v131, v132, vcc
	v_mul_f32_e32 v132, 0x4b800000, v130
	v_cmp_gt_f32_e64 s[0:1], s1, v130
	v_pk_fma_f32 v[112:113], v[112:113], v[28:29], v[120:121]
	v_pk_fma_f32 v[104:105], v[104:105], v[20:21], v[116:117]
	v_pk_fma_f32 v[108:109], v[108:109], v[32:33], v[128:129]
	v_pk_fma_f32 v[100:101], v[100:101], v[24:25], v[124:125]
	v_pk_fma_f32 v[110:111], v[110:111], v[26:27], v[118:119]
	v_pk_fma_f32 v[102:103], v[102:103], v[18:19], v[114:115]
	v_pk_fma_f32 v[106:107], v[106:107], v[30:31], v[126:127]
	v_pk_fma_f32 v[98:99], v[98:99], v[22:23], v[122:123]
	v_rsq_f32_e32 v131, v131
	v_cndmask_b32_e64 v130, v130, v132, s[0:1]
	v_pk_add_f32 v[98:99], v[98:99], v[106:107]
	v_pk_add_f32 v[102:103], v[102:103], v[110:111]
	v_pk_add_f32 v[100:101], v[100:101], v[108:109]
	v_pk_add_f32 v[104:105], v[104:105], v[112:113]
	v_rsq_f32_e32 v132, v130
	v_pk_add_f32 v[100:101], v[104:105], v[100:101]
	v_pk_add_f32 v[98:99], v[102:103], v[98:99]
	v_mul_f32_e32 v130, 0x45800000, v131
	v_add_f32_e32 v98, v98, v99
	v_add_f32_e32 v99, v100, v101
	v_add_f32_e32 v98, v98, v99
	v_mov_b32_e32 v99, v98
	v_pk_mul_f32 v[90:91], v[90:91], v[38:39]
	v_pk_mul_f32 v[94:95], v[94:95], v[46:47]
	v_pk_mul_f32 v[82:83], v[82:83], v[34:35]
	v_pk_mul_f32 v[86:87], v[86:87], v[42:43]
	v_cndmask_b32_e32 v130, v131, v130, vcc
	v_mul_f32_e32 v131, 0x45800000, v132
	v_permlane32_swap_b32_e32 v98, v99
	v_pk_fma_f32 v[78:79], v[78:79], v[26:27], v[86:87]
	v_pk_fma_f32 v[70:71], v[70:71], v[18:19], v[82:83]
	v_pk_fma_f32 v[74:75], v[74:75], v[30:31], v[94:95]
	v_pk_fma_f32 v[66:67], v[66:67], v[22:23], v[90:91]
	v_cndmask_b32_e64 v131, v132, v131, s[0:1]
	v_add_f32_e32 v98, v98, v99
	v_pk_add_f32 v[66:67], v[66:67], v[74:75]
	v_pk_add_f32 v[70:71], v[70:71], v[78:79]
	v_mul_f32_e32 v139, v160, v130
	v_mul_f32_e32 v98, v98, v131
	v_pk_add_f32 v[66:67], v[70:71], v[66:67]
	v_cmp_gt_u32_e32 vcc, 32, v1
	v_add_f32_e32 v66, v66, v67
	v_pk_mul_f32 v[92:93], v[92:93], v[40:41]
	v_cndmask_b32_e32 v67, v98, v139, vcc
	v_add_f32_e32 v67, s12, v67
	v_pk_mul_f32 v[96:97], v[96:97], v[48:49]
	v_pk_mul_f32 v[84:85], v[84:85], v[36:37]
	v_pk_mul_f32 v[88:89], v[88:89], v[44:45]
	v_mul_f32_e32 v67, 0xbfb8aa3b, v67
	v_pk_fma_f32 v[80:81], v[80:81], v[28:29], v[88:89]
	v_pk_fma_f32 v[72:73], v[72:73], v[20:21], v[84:85]
	v_pk_fma_f32 v[76:77], v[76:77], v[32:33], v[96:97]
	v_pk_fma_f32 v[68:69], v[68:69], v[24:25], v[92:93]
	v_exp_f32_e32 v70, v67
	v_pk_add_f32 v[68:69], v[68:69], v[76:77]
	v_pk_add_f32 v[72:73], v[72:73], v[80:81]
	v_cmp_lt_i32_e64 s[0:1], 0, v151
	v_pk_add_f32 v[68:69], v[72:73], v[68:69]
	v_mov_b32_e32 v137, v136
	v_add_f32_e32 v67, v68, v69
	v_add_f32_e32 v67, v66, v67
	v_add_f32_e32 v66, 1.0, v70
	v_rcp_f32_e32 v66, v66
	v_mov_b32_e32 v69, 0xff800000
	v_mov_b32_e32 v138, v133
	v_mov_b32_e32 v68, v67
	v_cndmask_b32_e64 v70, v69, v66, s[0:1]
	v_mbcnt_lo_u32_b32 v66, -1, 0
	v_mbcnt_hi_u32_b32 v66, -1, v66
	v_permlane32_swap_b32_e32 v136, v137
	v_permlane32_swap_b32_e32 v133, v138
	v_permlane32_swap_b32_e32 v67, v68
	v_and_b32_e32 v86, 64, v66
	s_mov_b32 s14, 8
	s_mov_b32 s13, 0
	v_mov_b32_e32 v66, 0
	s_waitcnt lgkmcnt(0)
.Ltopk_loop:
	v_max_f32_dpp v72, v70, v70 quad_perm:[1,0,3,2] row_mask:0xf bank_mask:0xf bound_ctrl:1
	s_nop 1
	v_max_f32_dpp v72, v72, v72 quad_perm:[2,3,0,1] row_mask:0xf bank_mask:0xf bound_ctrl:1
	s_nop 1
	v_max_f32_dpp v72, v72, v72 row_half_mirror row_mask:0xf bank_mask:0xf bound_ctrl:1
	s_nop 1
	v_max_f32_dpp v72, v72, v72 row_ror:8 row_mask:0xf bank_mask:0xf bound_ctrl:1
	v_mov_b32_e32 v73, v72
	s_nop 1
	v_permlane16_swap_b32_e32 v72, v73
	v_max_f32_e32 v72, v72, v73
	v_mov_b32_e32 v73, v72
	s_nop 1
	v_permlane32_swap_b32_e32 v72, v73
	v_max_f32_e32 v72, v72, v73
	v_cmp_eq_f32_e64 s[0:1], v70, v72
	s_ff1_i32_b64 s4, s[0:1]
	s_nop 0
	v_readlane_b32 s5, v151, s4
	v_cmp_eq_u32_e64 s[0:1], s4, v1
	s_add_i32 s13, s13, 1
	s_min_i32 s5, s5, s14
	s_sub_i32 s14, s14, s5
	v_mov_b32_e32 v73, s5
	v_cndmask_b32_e64 v70, v70, v69, s[0:1]
	v_cndmask_b32_e64 v66, v66, v73, s[0:1]
	s_cmp_lt_i32 s14, 1
	s_cbranch_scc1 .Ltopk_done
	s_cmp_lt_u32 s13, 8
	s_cbranch_scc1 .Ltopk_loop
.Ltopk_done:
	v_add_f32_e32 v69, v133, v138
	v_add_f32_e32 v67, v67, v68
	v_mul_f32_e32 v69, v69, v130
	v_mul_f32_e32 v67, v67, v131
	v_add_f32_e32 v68, v136, v137
	v_cndmask_b32_e32 v67, v67, v69, vcc
	v_add_f32_e32 v67, v68, v67
	v_mul_f32_e32 v68, 0x3e000000, v67
	v_mov_b32_e32 v69, 0xff800000
	v_cmp_lt_i32_e64 s[0:1], 0, v66
	s_mov_b32 s4, 0x3e000000
	v_cvt_f32_u32_e32 v66, v66
	v_cndmask_b32_e64 v68, v69, v68, s[0:1]
	v_cvt_pk_bf16_f32 v9, v8, v9
	v_cvt_pk_bf16_f32 v8, v6, v7
	v_max_f32_dpp v68, v68, v68 quad_perm:[1,0,3,2] row_mask:0xf bank_mask:0xf bound_ctrl:1
	v_cvt_pk_bf16_f32 v6, v2, v3
	s_nop 0
	v_max_f32_dpp v68, v68, v68 quad_perm:[2,3,0,1] row_mask:0xf bank_mask:0xf bound_ctrl:1
	v_cvt_pk_bf16_f32 v7, v4, v5
	s_nop 0
	v_max_f32_dpp v68, v68, v68 row_half_mirror row_mask:0xf bank_mask:0xf bound_ctrl:1
	v_cvt_pk_bf16_f32 v91, v16, v17
	v_cvt_pk_bf16_f32 v90, v14, v15
	v_max_f32_dpp v68, v68, v68 row_ror:8 row_mask:0xf bank_mask:0xf bound_ctrl:1
	v_mov_b32_e32 v69, v68
	s_nop 1
	v_permlane16_swap_b32_e32 v68, v69
	v_max_f32_e32 v68, v68, v69
	v_mov_b32_e32 v69, v68
	s_nop 1
	v_permlane32_swap_b32_e32 v68, v69
	v_max_f32_e32 v68, v68, v69
	v_fma_f32 v67, v67, s4, -v68
	v_mul_f32_e32 v67, 0x3fb8aa3b, v67
	v_exp_f32_e32 v67, v67
	v_cvt_pk_bf16_f32 v89, v12, v13
	v_cvt_pk_bf16_f32 v88, v10, v11
	v_mul_f32_e32 v66, v67, v66
	v_cndmask_b32_e64 v66, 0, v66, s[0:1]
	v_cvt_pk_bf16_f32 v57, v56, v57
	v_cvt_pk_bf16_f32 v56, v54, v55
	v_add_f32_dpp v67, v66, v66 quad_perm:[1,0,3,2] row_mask:0xf bank_mask:0xf bound_ctrl:1
	v_cvt_pk_bf16_f32 v54, v50, v51
	v_cvt_pk_bf16_f32 v50, v58, v59
	v_add_f32_dpp v67, v67, v67 quad_perm:[2,3,0,1] row_mask:0xf bank_mask:0xf bound_ctrl:1
	v_cvt_pk_bf16_f32 v55, v52, v53
	s_nop 0
	v_add_f32_dpp v67, v67, v67 row_half_mirror row_mask:0xf bank_mask:0xf bound_ctrl:1
	v_cvt_pk_bf16_f32 v53, v64, v65
	v_cvt_pk_bf16_f32 v52, v62, v63
	v_add_f32_dpp v67, v67, v67 row_ror:8 row_mask:0xf bank_mask:0xf bound_ctrl:1
	v_mov_b32_e32 v68, v67
	s_nop 1
	v_permlane16_swap_b32_e32 v67, v68
	v_add_f32_e32 v67, v67, v68
	v_mov_b32_e32 v68, v67
	s_nop 1
	v_permlane32_swap_b32_e32 v67, v68
	v_add_f32_e32 v67, v67, v68
	v_rcp_f32_e32 v67, v67
	v_cvt_pk_bf16_f32 v51, v60, v61
	v_cvt_pk_bf16_f32 v25, v24, v25
	v_cvt_pk_bf16_f32 v24, v22, v23
	v_mul_f32_e32 v66, v66, v67
	v_cndmask_b32_e32 v67, v131, v130, vcc
	v_mul_f32_e32 v66, v67, v66
	ds_write_b32 v173, v66 offset:768
	s_waitcnt lgkmcnt(0)
	ds_read_b128 v[82:85], v212 offset:27648
	ds_read_b128 v[92:95], v212 offset:28672
	ds_read_b128 v[96:99], v212 offset:31744
	ds_read_b128 v[100:103], v212 offset:32768
	s_waitcnt lgkmcnt(3)
	v_mfma_f32_32x32x16_bf16 v[66:81], v[6:9], v[82:85], 0
	ds_read_b128 v[104:107], v212 offset:29696
	ds_read_b32 v87, v135 offset:34816
	v_cvt_pk_bf16_f32 v23, v20, v21
	v_cvt_pk_bf16_f32 v22, v18, v19
	v_cvt_pk_bf16_f32 v119, v32, v33
	v_cvt_pk_bf16_f32 v118, v30, v31
	v_cvt_pk_bf16_f32 v117, v28, v29
	s_waitcnt lgkmcnt(3)
	v_mfma_f32_32x32x16_bf16 v[2:17], v[6:9], v[96:99], 0
	v_cvt_pk_bf16_f32 v116, v26, v27
	v_cvt_pk_bf16_f32 v41, v40, v41
	v_cvt_pk_bf16_f32 v40, v38, v39
	v_cvt_pk_bf16_f32 v39, v36, v37
	v_cvt_pk_bf16_f32 v38, v34, v35
	v_cvt_pk_bf16_f32 v37, v48, v49
	v_cvt_pk_bf16_f32 v36, v46, v47
	v_mfma_f32_32x32x16_bf16 v[66:81], v[88:91], v[92:95], v[66:81]
	v_cvt_pk_bf16_f32 v35, v44, v45
	v_cvt_pk_bf16_f32 v34, v42, v43
	s_waitcnt lgkmcnt(2)
	v_mfma_f32_32x32x16_bf16 v[2:17], v[88:91], v[100:103], v[2:17]
	ds_read_b128 v[88:91], v212 offset:30720
	ds_read_b128 v[108:111], v212 offset:33792
	s_waitcnt lgkmcnt(3)
	v_mfma_f32_32x32x16_bf16 v[66:81], v[54:57], v[104:107], v[66:81]
	s_waitcnt lgkmcnt(0)
	v_mfma_f32_32x32x16_bf16 v[2:17], v[54:57], v[108:111], v[2:17]
	ds_read_b128 v[112:115], v212 offset:34816
	v_mfma_f32_32x32x16_bf16 v[66:81], v[50:53], v[88:91], v[66:81]
	s_waitcnt lgkmcnt(0)
	v_mfma_f32_32x32x16_bf16 v[2:17], v[50:53], v[112:115], v[2:17]
	v_mfma_f32_32x32x16_bf16 v[50:65], v[22:25], v[82:85], 0
	v_mfma_f32_32x32x16_bf16 v[18:33], v[22:25], v[96:99], 0
	v_mfma_f32_32x32x16_bf16 v[50:65], v[116:119], v[92:95], v[50:65]
	v_mfma_f32_32x32x16_bf16 v[18:33], v[116:119], v[100:103], v[18:33]
	v_mfma_f32_32x32x16_bf16 v[50:65], v[38:41], v[104:107], v[50:65]
	v_mfma_f32_32x32x16_bf16 v[18:33], v[38:41], v[108:111], v[18:33]
	ds_read_b128 v[38:41], v134 offset:896
	ds_read_b128 v[42:45], v134 offset:928
	v_mfma_f32_32x32x16_bf16 v[50:65], v[34:37], v[88:91], v[50:65]
	v_mfma_f32_32x32x16_bf16 v[18:33], v[34:37], v[112:115], v[18:33]
	ds_read_b128 v[34:37], v134 offset:960
	ds_read_b128 v[46:49], v134 offset:992
	ds_read_b128 v[82:85], v134 offset:768
	ds_read_b128 v[88:91], v134 offset:800
	ds_read_b128 v[92:95], v134 offset:832
	ds_read_b128 v[96:99], v134 offset:864
	s_waitcnt lgkmcnt(6)
	s_nop 3
	v_pk_mul_f32 v[54:55], v[42:43], v[54:55]
	s_waitcnt lgkmcnt(4)
	v_pk_mul_f32 v[62:63], v[46:47], v[62:63]
	v_pk_mul_f32 v[56:57], v[44:45], v[56:57]
	v_pk_mul_f32 v[64:65], v[48:49], v[64:65]
	v_pk_mul_f32 v[52:53], v[40:41], v[52:53]
	v_pk_mul_f32 v[60:61], v[36:37], v[60:61]
	v_pk_mul_f32 v[58:59], v[34:35], v[58:59]
	v_pk_mul_f32 v[50:51], v[38:39], v[50:51]
	v_pk_mul_f32 v[22:23], v[42:43], v[22:23]
	v_pk_mul_f32 v[30:31], v[46:47], v[30:31]
	v_pk_mul_f32 v[24:25], v[44:45], v[24:25]
	v_pk_mul_f32 v[32:33], v[48:49], v[32:33]
	v_pk_mul_f32 v[20:21], v[40:41], v[20:21]
	v_pk_mul_f32 v[28:29], v[36:37], v[28:29]
	v_pk_mul_f32 v[26:27], v[34:35], v[26:27]
	v_pk_mul_f32 v[18:19], v[38:39], v[18:19]
	s_waitcnt lgkmcnt(1)
	v_pk_fma_f32 v[58:59], v[92:93], v[74:75], v[58:59]
	v_pk_fma_f32 v[60:61], v[94:95], v[76:77], v[60:61]
	v_pk_fma_f32 v[52:53], v[84:85], v[68:69], v[52:53]
	s_waitcnt lgkmcnt(0)
	v_pk_fma_f32 v[64:65], v[98:99], v[80:81], v[64:65]
	v_pk_fma_f32 v[56:57], v[90:91], v[72:73], v[56:57]
	v_pk_fma_f32 v[62:63], v[96:97], v[78:79], v[62:63]
	v_pk_fma_f32 v[54:55], v[88:89], v[70:71], v[54:55]
	v_pk_fma_f32 v[50:51], v[82:83], v[66:67], v[50:51]
	v_pk_fma_f32 v[10:11], v[92:93], v[10:11], v[26:27]
	v_pk_fma_f32 v[12:13], v[94:95], v[12:13], v[28:29]
	v_pk_fma_f32 v[4:5], v[84:85], v[4:5], v[20:21]
	v_pk_fma_f32 v[16:17], v[98:99], v[16:17], v[32:33]
	v_pk_fma_f32 v[8:9], v[90:91], v[8:9], v[24:25]
	v_pk_fma_f32 v[14:15], v[96:97], v[14:15], v[30:31]
	v_pk_fma_f32 v[6:7], v[88:89], v[6:7], v[22:23]
	v_pk_fma_f32 v[2:3], v[82:83], v[2:3], v[18:19]
	v_pk_add_f32 v[54:55], v[54:55], v[62:63]
	v_pk_add_f32 v[56:57], v[56:57], v[64:65]
	v_pk_add_f32 v[52:53], v[52:53], v[60:61]
	v_pk_add_f32 v[50:51], v[50:51], v[58:59]
	v_pk_add_f32 v[6:7], v[6:7], v[14:15]
	v_pk_add_f32 v[8:9], v[8:9], v[16:17]
	v_pk_add_f32 v[4:5], v[4:5], v[12:13]
	v_pk_add_f32 v[2:3], v[2:3], v[10:11]
	v_pk_add_f32 v[52:53], v[52:53], v[56:57]
	v_pk_add_f32 v[50:51], v[50:51], v[54:55]
	v_pk_add_f32 v[4:5], v[4:5], v[8:9]
	v_pk_add_f32 v[2:3], v[2:3], v[6:7]
	v_add_f32_e32 v50, v50, v51
	v_add_f32_e32 v51, v52, v53
	v_add_f32_e32 v2, v2, v3
	v_add_f32_e32 v3, v4, v5
	v_add_f32_e32 v50, v50, v51
	v_add_f32_e32 v2, v2, v3
	v_mov_b32_e32 v3, v50
	v_mov_b32_e32 v4, v2
	s_nop 0
	v_permlane32_swap_b32_e32 v50, v3
	v_permlane32_swap_b32_e32 v2, v4
	v_add_f32_e32 v3, v50, v3
	v_add_f32_e32 v2, v2, v4
	v_cndmask_b32_e32 v2, v2, v3, vcc
	v_add_f32_e32 v3, v87, v2
	v_cmp_eq_u32_e32 vcc, 0, v1
	s_nop 0
	v_max_f32_dpp v2, v3, v3 quad_perm:[1,0,3,2] row_mask:0xf bank_mask:0xf bound_ctrl:1
	s_nop 1
	v_max_f32_dpp v2, v2, v2 quad_perm:[2,3,0,1] row_mask:0xf bank_mask:0xf bound_ctrl:1
	s_nop 1
	v_max_f32_dpp v2, v2, v2 row_half_mirror row_mask:0xf bank_mask:0xf bound_ctrl:1
	s_nop 1
	v_max_f32_dpp v2, v2, v2 row_ror:8 row_mask:0xf bank_mask:0xf bound_ctrl:1
	v_mov_b32_e32 v4, v2
	s_nop 1
	v_permlane16_swap_b32_e32 v2, v4
	v_max_f32_e32 v2, v2, v4
	v_mov_b32_e32 v4, v2
	s_nop 1
	v_permlane32_swap_b32_e32 v2, v4
	v_max_f32_e32 v2, v2, v4
	v_sub_f32_e32 v4, v3, v2
	v_mul_f32_e32 v4, 0x3fb8aa3b, v4
	v_exp_f32_e32 v4, v4
	s_nop 1
	v_add_f32_dpp v4, v4, v4 quad_perm:[1,0,3,2] row_mask:0xf bank_mask:0xf bound_ctrl:1
	s_nop 1
	v_add_f32_dpp v4, v4, v4 quad_perm:[2,3,0,1] row_mask:0xf bank_mask:0xf bound_ctrl:1
	s_nop 1
	v_add_f32_dpp v4, v4, v4 row_half_mirror row_mask:0xf bank_mask:0xf bound_ctrl:1
	s_nop 1
	v_add_f32_dpp v4, v4, v4 row_ror:8 row_mask:0xf bank_mask:0xf bound_ctrl:1
	v_mov_b32_e32 v5, v4
	s_nop 1
	v_permlane16_swap_b32_e32 v4, v5
	v_add_f32_e32 v4, v4, v5
	v_and_or_b32 v5, s3, 63, v86
	v_lshlrev_b32_e32 v5, 2, v5
	ds_bpermute_b32 v3, v5, v3
	v_mov_b32_e32 v5, v4
	s_nop 1
	v_permlane32_swap_b32_e32 v4, v5
	s_and_saveexec_b64 s[4:5], vcc
	s_cbranch_execz .LBB1_12
	v_add_f32_e32 v1, v4, v5
	s_mov_b32 s0, 0x800000
	v_cmp_gt_f32_e32 vcc, s0, v1
	s_mov_b32 s0, 0x3f317217
	s_nop 0
	v_cndmask_b32_e64 v4, 0, 32, vcc
	v_ldexp_f32 v1, v1, v4
	v_log_f32_e32 v1, v1
	s_nop 0
	v_mul_f32_e32 v4, 0x3f317217, v1
	v_fma_f32 v4, v1, s0, -v4
	v_fmamk_f32 v4, v1, 0x3377d1cf, v4
	s_mov_b32 s0, 0x7f800000
	v_fmac_f32_e32 v4, 0x3f317217, v1
	v_cmp_lt_f32_e64 s[0:1], |v1|, s0
	s_nop 1
	v_cndmask_b32_e64 v1, v1, v4, s[0:1]
	v_mov_b32_e32 v4, 0x41b17218
	v_cndmask_b32_e32 v4, 0, v4, vcc
	v_sub_f32_e32 v1, v1, v4
	v_add_f32_e32 v1, v2, v1
	s_waitcnt lgkmcnt(0)
	v_sub_f32_e32 v1, v1, v3
	ds_write_b32 v172, v1
